# speedup vs baseline: 1.0013x; 1.0013x over previous
.LBB1_30:
	s_load_dwordx8 s[8:15], s[0:1], 0x10
	s_load_dwordx2 s[16:17], s[0:1], 0x30
	s_bitcmp1_b32 s18, 6
	s_cselect_b32 s24, 0x60, 0
	s_lshr_b32 s4, s18, 1
	s_and_b32 s23, s4, 0x7fffffc0
	v_lshrrev_b32_e32 v98, 5, v1
	s_cmpk_lt_u32 s18, 0x200
	v_and_b32_e32 v1, 31, v0
	v_mov_b32_e32 v2, 0
	s_cselect_b64 s[4:5], -1, 0
	s_cmpk_gt_u32 s18, 0x1ff
	v_mov_b32_e32 v3, 0
	v_mov_b32_e32 v4, 0
	v_mov_b32_e32 v5, 0
	v_mov_b32_e32 v6, 0
	v_mov_b32_e32 v7, 0
	v_mov_b32_e32 v8, 0
	v_mov_b32_e32 v9, 0
	v_mov_b32_e32 v10, 0
	v_mov_b32_e32 v11, 0
	v_mov_b32_e32 v12, 0
	v_mov_b32_e32 v13, 0
	v_mov_b32_e32 v14, 0
	v_mov_b32_e32 v15, 0
	v_mov_b32_e32 v16, 0
	v_mov_b32_e32 v17, 0
	v_mov_b32_e32 v50, 0
	v_mov_b32_e32 v51, 0
	v_mov_b32_e32 v52, 0
	v_mov_b32_e32 v53, 0
	v_mov_b32_e32 v54, 0
	v_mov_b32_e32 v55, 0
	v_mov_b32_e32 v56, 0
	v_mov_b32_e32 v57, 0
	v_mov_b32_e32 v58, 0
	v_mov_b32_e32 v59, 0
	v_mov_b32_e32 v60, 0
	v_mov_b32_e32 v61, 0
	v_mov_b32_e32 v62, 0
	v_mov_b32_e32 v63, 0
	v_mov_b32_e32 v64, 0
	v_mov_b32_e32 v65, 0
	v_mov_b32_e32 v18, 0
	v_mov_b32_e32 v19, 0
	v_mov_b32_e32 v20, 0
	v_mov_b32_e32 v21, 0
	v_mov_b32_e32 v22, 0
	v_mov_b32_e32 v23, 0
	v_mov_b32_e32 v24, 0
	v_mov_b32_e32 v25, 0
	v_mov_b32_e32 v26, 0
	v_mov_b32_e32 v27, 0
	v_mov_b32_e32 v28, 0
	v_mov_b32_e32 v29, 0
	v_mov_b32_e32 v30, 0
	v_mov_b32_e32 v31, 0
	v_mov_b32_e32 v32, 0
	v_mov_b32_e32 v33, 0
	v_mov_b32_e32 v66, 0
	v_mov_b32_e32 v67, 0
	v_mov_b32_e32 v68, 0
	v_mov_b32_e32 v69, 0
	v_mov_b32_e32 v70, 0
	v_mov_b32_e32 v71, 0
	v_mov_b32_e32 v72, 0
	v_mov_b32_e32 v73, 0
	v_mov_b32_e32 v74, 0
	v_mov_b32_e32 v75, 0
	v_mov_b32_e32 v76, 0
	v_mov_b32_e32 v77, 0
	v_mov_b32_e32 v78, 0
	v_mov_b32_e32 v79, 0
	v_mov_b32_e32 v80, 0
	v_mov_b32_e32 v81, 0
	v_mov_b32_e32 v34, 0
	v_mov_b32_e32 v35, 0
	v_mov_b32_e32 v36, 0
	v_mov_b32_e32 v37, 0
	v_mov_b32_e32 v38, 0
	v_mov_b32_e32 v39, 0
	v_mov_b32_e32 v40, 0
	v_mov_b32_e32 v41, 0
	v_mov_b32_e32 v42, 0
	v_mov_b32_e32 v43, 0
	v_mov_b32_e32 v44, 0
	v_mov_b32_e32 v45, 0
	v_mov_b32_e32 v46, 0
	v_mov_b32_e32 v47, 0
	v_mov_b32_e32 v48, 0
	v_mov_b32_e32 v49, 0
	v_mov_b32_e32 v82, 0
	v_mov_b32_e32 v83, 0
	v_mov_b32_e32 v84, 0
	v_mov_b32_e32 v85, 0
	v_mov_b32_e32 v86, 0
	v_mov_b32_e32 v87, 0
	v_mov_b32_e32 v88, 0
	v_mov_b32_e32 v89, 0
	v_mov_b32_e32 v90, 0
	v_mov_b32_e32 v91, 0
	v_mov_b32_e32 v92, 0
	v_mov_b32_e32 v93, 0
	v_mov_b32_e32 v94, 0
	v_mov_b32_e32 v95, 0
	v_mov_b32_e32 v96, 0
	v_mov_b32_e32 v97, 0
	v_or_b32_e32 v99, s24, v1
	v_or_b32_e32 v100, s23, v1
	s_cbranch_scc1 .LBB1_35
	v_bfe_u32 v109, v0, 2, 2
	v_xor_b32_e32 v110, v109, v98
	v_xor_b32_e32 v111, 2, v110
	v_lshlrev_b32_e32 v110, 4, v110
	v_lshlrev_b32_e32 v111, 4, v111
	v_lshl_add_u32 v101, v99, 6, v110
	v_lshl_add_u32 v102, v99, 6, v111
	v_lshl_add_u32 v103, v100, 6, v110
	v_lshl_add_u32 v104, v100, 6, v111
	v_add_u32_e32 v101, 0x800, v101
	v_add_u32_e32 v102, 0x800, v102
	v_add_u32_e32 v103, 0x3800, v103
	v_add_u32_e32 v104, 0x3800, v104
	v_add_u32_e32 v105, 0xe000, v101
	v_add_u32_e32 v106, 0xe000, v102
	v_add_u32_e32 v107, 0xe000, v103
	v_add_u32_e32 v108, 0xe000, v104
	v_add_u32_e32 v152, 0x1c000, v101
	v_add_u32_e32 v153, 0x1c000, v102
	v_add_u32_e32 v154, 0x1c000, v103
	v_add_u32_e32 v155, 0x1c000, v104
	s_cmp_lt_u32 s2, 64
	s_cbranch_scc1 .Lqkv_cv
	s_barrier
	ds_read_b128 v[124:127], v103
	ds_read_b128 v[112:115], v101
	ds_read_b128 v[128:131], v103 offset:2048
	ds_read_b128 v[116:119], v101 offset:2048
	ds_read_b128 v[120:123], v101 offset:4096
	s_waitcnt lgkmcnt(0)
	v_mfma_f32_32x32x16_f16 v[82:97], v[112:115], v[124:127], v[82:97]
	ds_read_b128 v[144:147], v104
	ds_read_b128 v[132:135], v102
	v_mfma_f32_32x32x16_f16 v[34:49], v[112:115], v[128:131], v[34:49]
	ds_read_b128 v[148:151], v104 offset:2048
	ds_read_b128 v[136:139], v102 offset:2048
	v_mfma_f32_32x32x16_f16 v[66:81], v[116:119], v[124:127], v[66:81]
	ds_read_b128 v[140:143], v102 offset:4096
	v_mfma_f32_32x32x16_f16 v[18:33], v[116:119], v[128:131], v[18:33]
	v_mfma_f32_32x32x16_f16 v[50:65], v[120:123], v[124:127], v[50:65]
	v_mfma_f32_32x32x16_f16 v[2:17], v[120:123], v[128:131], v[2:17]
	s_waitcnt lgkmcnt(0)
	s_barrier
	v_mfma_f32_32x32x16_f16 v[82:97], v[132:135], v[144:147], v[82:97]
	ds_read_b128 v[124:127], v103 offset:28672
	ds_read_b128 v[112:115], v101 offset:28672
	v_mfma_f32_32x32x16_f16 v[34:49], v[132:135], v[148:151], v[34:49]
	ds_read_b128 v[128:131], v103 offset:30720
	ds_read_b128 v[116:119], v101 offset:30720
	v_mfma_f32_32x32x16_f16 v[66:81], v[136:139], v[144:147], v[66:81]
	ds_read_b128 v[120:123], v101 offset:32768
	v_mfma_f32_32x32x16_f16 v[18:33], v[136:139], v[148:151], v[18:33]
	v_mfma_f32_32x32x16_f16 v[50:65], v[140:143], v[144:147], v[50:65]
	v_mfma_f32_32x32x16_f16 v[2:17], v[140:143], v[148:151], v[2:17]
	s_waitcnt lgkmcnt(0)
	v_mfma_f32_32x32x16_f16 v[82:97], v[112:115], v[124:127], v[82:97]
	ds_read_b128 v[144:147], v104 offset:28672
	ds_read_b128 v[132:135], v102 offset:28672
	v_mfma_f32_32x32x16_f16 v[34:49], v[112:115], v[128:131], v[34:49]
	ds_read_b128 v[148:151], v104 offset:30720
	ds_read_b128 v[136:139], v102 offset:30720
	v_mfma_f32_32x32x16_f16 v[66:81], v[116:119], v[124:127], v[66:81]
	ds_read_b128 v[140:143], v102 offset:32768
	v_mfma_f32_32x32x16_f16 v[18:33], v[116:119], v[128:131], v[18:33]
	v_mfma_f32_32x32x16_f16 v[50:65], v[120:123], v[124:127], v[50:65]
	v_mfma_f32_32x32x16_f16 v[2:17], v[120:123], v[128:131], v[2:17]
	s_waitcnt lgkmcnt(0)
	s_barrier
	v_mfma_f32_32x32x16_f16 v[82:97], v[132:135], v[144:147], v[82:97]
	ds_read_b128 v[124:127], v107
	ds_read_b128 v[112:115], v105
	v_mfma_f32_32x32x16_f16 v[34:49], v[132:135], v[148:151], v[34:49]
	ds_read_b128 v[128:131], v107 offset:2048
	ds_read_b128 v[116:119], v105 offset:2048
	v_mfma_f32_32x32x16_f16 v[66:81], v[136:139], v[144:147], v[66:81]
	ds_read_b128 v[120:123], v105 offset:4096
	v_mfma_f32_32x32x16_f16 v[18:33], v[136:139], v[148:151], v[18:33]
	v_mfma_f32_32x32x16_f16 v[50:65], v[140:143], v[144:147], v[50:65]
	v_mfma_f32_32x32x16_f16 v[2:17], v[140:143], v[148:151], v[2:17]
	s_waitcnt lgkmcnt(0)
	v_mfma_f32_32x32x16_f16 v[82:97], v[112:115], v[124:127], v[82:97]
	ds_read_b128 v[144:147], v108
	ds_read_b128 v[132:135], v106
	v_mfma_f32_32x32x16_f16 v[34:49], v[112:115], v[128:131], v[34:49]
	ds_read_b128 v[148:151], v108 offset:2048
	ds_read_b128 v[136:139], v106 offset:2048
	v_mfma_f32_32x32x16_f16 v[66:81], v[116:119], v[124:127], v[66:81]
	ds_read_b128 v[140:143], v106 offset:4096
	v_mfma_f32_32x32x16_f16 v[18:33], v[116:119], v[128:131], v[18:33]
	v_mfma_f32_32x32x16_f16 v[50:65], v[120:123], v[124:127], v[50:65]
	v_mfma_f32_32x32x16_f16 v[2:17], v[120:123], v[128:131], v[2:17]
	s_waitcnt lgkmcnt(0)
	s_barrier
	v_mfma_f32_32x32x16_f16 v[82:97], v[132:135], v[144:147], v[82:97]
	ds_read_b128 v[124:127], v107 offset:28672
	ds_read_b128 v[112:115], v105 offset:28672
	v_mfma_f32_32x32x16_f16 v[34:49], v[132:135], v[148:151], v[34:49]
	ds_read_b128 v[128:131], v107 offset:30720
	ds_read_b128 v[116:119], v105 offset:30720
	v_mfma_f32_32x32x16_f16 v[66:81], v[136:139], v[144:147], v[66:81]
	ds_read_b128 v[120:123], v105 offset:32768
	v_mfma_f32_32x32x16_f16 v[18:33], v[136:139], v[148:151], v[18:33]
	v_mfma_f32_32x32x16_f16 v[50:65], v[140:143], v[144:147], v[50:65]
	v_mfma_f32_32x32x16_f16 v[2:17], v[140:143], v[148:151], v[2:17]
	s_waitcnt lgkmcnt(0)
	v_mfma_f32_32x32x16_f16 v[82:97], v[112:115], v[124:127], v[82:97]
	ds_read_b128 v[144:147], v108 offset:28672
	ds_read_b128 v[132:135], v106 offset:28672
	v_mfma_f32_32x32x16_f16 v[34:49], v[112:115], v[128:131], v[34:49]
	ds_read_b128 v[148:151], v108 offset:30720
	ds_read_b128 v[136:139], v106 offset:30720
	v_mfma_f32_32x32x16_f16 v[66:81], v[116:119], v[124:127], v[66:81]
	ds_read_b128 v[140:143], v106 offset:32768
	v_mfma_f32_32x32x16_f16 v[18:33], v[116:119], v[128:131], v[18:33]
	v_mfma_f32_32x32x16_f16 v[50:65], v[120:123], v[124:127], v[50:65]
	v_mfma_f32_32x32x16_f16 v[2:17], v[120:123], v[128:131], v[2:17]
	s_waitcnt lgkmcnt(0)
	s_barrier
	v_mfma_f32_32x32x16_f16 v[82:97], v[132:135], v[144:147], v[82:97]
	ds_read_b128 v[124:127], v154
	ds_read_b128 v[112:115], v152
	v_mfma_f32_32x32x16_f16 v[34:49], v[132:135], v[148:151], v[34:49]
	ds_read_b128 v[128:131], v154 offset:2048
	ds_read_b128 v[116:119], v152 offset:2048
	v_mfma_f32_32x32x16_f16 v[66:81], v[136:139], v[144:147], v[66:81]
	ds_read_b128 v[120:123], v152 offset:4096
	v_mfma_f32_32x32x16_f16 v[18:33], v[136:139], v[148:151], v[18:33]
	v_mfma_f32_32x32x16_f16 v[50:65], v[140:143], v[144:147], v[50:65]
	v_mfma_f32_32x32x16_f16 v[2:17], v[140:143], v[148:151], v[2:17]
	s_waitcnt lgkmcnt(0)
	v_mfma_f32_32x32x16_f16 v[82:97], v[112:115], v[124:127], v[82:97]
	ds_read_b128 v[144:147], v155
	ds_read_b128 v[132:135], v153
	v_mfma_f32_32x32x16_f16 v[34:49], v[112:115], v[128:131], v[34:49]
	ds_read_b128 v[148:151], v155 offset:2048
	ds_read_b128 v[136:139], v153 offset:2048
	v_mfma_f32_32x32x16_f16 v[66:81], v[116:119], v[124:127], v[66:81]
	ds_read_b128 v[140:143], v153 offset:4096
	v_mfma_f32_32x32x16_f16 v[18:33], v[116:119], v[128:131], v[18:33]
	v_mfma_f32_32x32x16_f16 v[50:65], v[120:123], v[124:127], v[50:65]
	v_mfma_f32_32x32x16_f16 v[2:17], v[120:123], v[128:131], v[2:17]
	s_waitcnt lgkmcnt(0)
	s_barrier
	v_mfma_f32_32x32x16_f16 v[82:97], v[132:135], v[144:147], v[82:97]
	ds_read_b128 v[124:127], v103
	ds_read_b128 v[112:115], v101
	v_mfma_f32_32x32x16_f16 v[34:49], v[132:135], v[148:151], v[34:49]
	ds_read_b128 v[128:131], v103 offset:2048
	ds_read_b128 v[116:119], v101 offset:2048
	v_mfma_f32_32x32x16_f16 v[66:81], v[136:139], v[144:147], v[66:81]
	ds_read_b128 v[120:123], v101 offset:4096
	v_mfma_f32_32x32x16_f16 v[18:33], v[136:139], v[148:151], v[18:33]
	v_mfma_f32_32x32x16_f16 v[50:65], v[140:143], v[144:147], v[50:65]
	v_mfma_f32_32x32x16_f16 v[2:17], v[140:143], v[148:151], v[2:17]
	s_waitcnt lgkmcnt(0)
	v_mfma_f32_32x32x16_f16 v[82:97], v[112:115], v[124:127], v[82:97]
	ds_read_b128 v[144:147], v104
	ds_read_b128 v[132:135], v102
	v_mfma_f32_32x32x16_f16 v[34:49], v[112:115], v[128:131], v[34:49]
	ds_read_b128 v[148:151], v104 offset:2048
	ds_read_b128 v[136:139], v102 offset:2048
	v_mfma_f32_32x32x16_f16 v[66:81], v[116:119], v[124:127], v[66:81]
	ds_read_b128 v[140:143], v102 offset:4096
	v_mfma_f32_32x32x16_f16 v[18:33], v[116:119], v[128:131], v[18:33]
	v_mfma_f32_32x32x16_f16 v[50:65], v[120:123], v[124:127], v[50:65]
	v_mfma_f32_32x32x16_f16 v[2:17], v[120:123], v[128:131], v[2:17]
	s_waitcnt lgkmcnt(0)
	s_barrier
	v_mfma_f32_32x32x16_f16 v[82:97], v[132:135], v[144:147], v[82:97]
	ds_read_b128 v[124:127], v103 offset:28672
	ds_read_b128 v[112:115], v101 offset:28672
	v_mfma_f32_32x32x16_f16 v[34:49], v[132:135], v[148:151], v[34:49]
	ds_read_b128 v[128:131], v103 offset:30720
	ds_read_b128 v[116:119], v101 offset:30720
	v_mfma_f32_32x32x16_f16 v[66:81], v[136:139], v[144:147], v[66:81]
	ds_read_b128 v[120:123], v101 offset:32768
	v_mfma_f32_32x32x16_f16 v[18:33], v[136:139], v[148:151], v[18:33]
	v_mfma_f32_32x32x16_f16 v[50:65], v[140:143], v[144:147], v[50:65]
	v_mfma_f32_32x32x16_f16 v[2:17], v[140:143], v[148:151], v[2:17]
	s_waitcnt lgkmcnt(0)
	v_mfma_f32_32x32x16_f16 v[82:97], v[112:115], v[124:127], v[82:97]
	ds_read_b128 v[144:147], v104 offset:28672
	ds_read_b128 v[132:135], v102 offset:28672
	v_mfma_f32_32x32x16_f16 v[34:49], v[112:115], v[128:131], v[34:49]
	ds_read_b128 v[148:151], v104 offset:30720
	ds_read_b128 v[136:139], v102 offset:30720
	v_mfma_f32_32x32x16_f16 v[66:81], v[116:119], v[124:127], v[66:81]
	ds_read_b128 v[140:143], v102 offset:32768
	v_mfma_f32_32x32x16_f16 v[18:33], v[116:119], v[128:131], v[18:33]
	v_mfma_f32_32x32x16_f16 v[50:65], v[120:123], v[124:127], v[50:65]
	v_mfma_f32_32x32x16_f16 v[2:17], v[120:123], v[128:131], v[2:17]
	s_waitcnt lgkmcnt(0)
	s_barrier
	v_mfma_f32_32x32x16_f16 v[82:97], v[132:135], v[144:147], v[82:97]
	ds_read_b128 v[124:127], v107
	ds_read_b128 v[112:115], v105
	v_mfma_f32_32x32x16_f16 v[34:49], v[132:135], v[148:151], v[34:49]
	ds_read_b128 v[128:131], v107 offset:2048
	ds_read_b128 v[116:119], v105 offset:2048
	v_mfma_f32_32x32x16_f16 v[66:81], v[136:139], v[144:147], v[66:81]
	ds_read_b128 v[120:123], v105 offset:4096
	v_mfma_f32_32x32x16_f16 v[18:33], v[136:139], v[148:151], v[18:33]
	v_mfma_f32_32x32x16_f16 v[50:65], v[140:143], v[144:147], v[50:65]
	v_mfma_f32_32x32x16_f16 v[2:17], v[140:143], v[148:151], v[2:17]
	s_waitcnt lgkmcnt(0)
	v_mfma_f32_32x32x16_f16 v[82:97], v[112:115], v[124:127], v[82:97]
	ds_read_b128 v[144:147], v108
	ds_read_b128 v[132:135], v106
	v_mfma_f32_32x32x16_f16 v[34:49], v[112:115], v[128:131], v[34:49]
	ds_read_b128 v[148:151], v108 offset:2048
	ds_read_b128 v[136:139], v106 offset:2048
	v_mfma_f32_32x32x16_f16 v[66:81], v[116:119], v[124:127], v[66:81]
	ds_read_b128 v[140:143], v106 offset:4096
	v_mfma_f32_32x32x16_f16 v[18:33], v[116:119], v[128:131], v[18:33]
	v_mfma_f32_32x32x16_f16 v[50:65], v[120:123], v[124:127], v[50:65]
	v_mfma_f32_32x32x16_f16 v[2:17], v[120:123], v[128:131], v[2:17]
	s_waitcnt lgkmcnt(0)
	s_barrier
	v_mfma_f32_32x32x16_f16 v[82:97], v[132:135], v[144:147], v[82:97]
	ds_read_b128 v[124:127], v107 offset:28672
	ds_read_b128 v[112:115], v105 offset:28672
	v_mfma_f32_32x32x16_f16 v[34:49], v[132:135], v[148:151], v[34:49]
	ds_read_b128 v[128:131], v107 offset:30720
	ds_read_b128 v[116:119], v105 offset:30720
	v_mfma_f32_32x32x16_f16 v[66:81], v[136:139], v[144:147], v[66:81]
	ds_read_b128 v[120:123], v105 offset:32768
	v_mfma_f32_32x32x16_f16 v[18:33], v[136:139], v[148:151], v[18:33]
	v_mfma_f32_32x32x16_f16 v[50:65], v[140:143], v[144:147], v[50:65]
	v_mfma_f32_32x32x16_f16 v[2:17], v[140:143], v[148:151], v[2:17]
	s_waitcnt lgkmcnt(0)
	v_mfma_f32_32x32x16_f16 v[82:97], v[112:115], v[124:127], v[82:97]
	ds_read_b128 v[144:147], v108 offset:28672
	ds_read_b128 v[132:135], v106 offset:28672
	v_mfma_f32_32x32x16_f16 v[34:49], v[112:115], v[128:131], v[34:49]
	ds_read_b128 v[148:151], v108 offset:30720
	ds_read_b128 v[136:139], v106 offset:30720
	v_mfma_f32_32x32x16_f16 v[66:81], v[116:119], v[124:127], v[66:81]
	ds_read_b128 v[140:143], v106 offset:32768
	v_mfma_f32_32x32x16_f16 v[18:33], v[116:119], v[128:131], v[18:33]
	v_mfma_f32_32x32x16_f16 v[50:65], v[120:123], v[124:127], v[50:65]
	v_mfma_f32_32x32x16_f16 v[2:17], v[120:123], v[128:131], v[2:17]
	s_waitcnt lgkmcnt(0)
	s_barrier
	v_mfma_f32_32x32x16_f16 v[82:97], v[132:135], v[144:147], v[82:97]
	ds_read_b128 v[124:127], v154
	ds_read_b128 v[112:115], v152
	v_mfma_f32_32x32x16_f16 v[34:49], v[132:135], v[148:151], v[34:49]
	ds_read_b128 v[128:131], v154 offset:2048
	ds_read_b128 v[116:119], v152 offset:2048
	v_mfma_f32_32x32x16_f16 v[66:81], v[136:139], v[144:147], v[66:81]
	ds_read_b128 v[120:123], v152 offset:4096
	v_mfma_f32_32x32x16_f16 v[18:33], v[136:139], v[148:151], v[18:33]
	v_mfma_f32_32x32x16_f16 v[50:65], v[140:143], v[144:147], v[50:65]
	v_mfma_f32_32x32x16_f16 v[2:17], v[140:143], v[148:151], v[2:17]
	s_waitcnt lgkmcnt(0)
	v_mfma_f32_32x32x16_f16 v[82:97], v[112:115], v[124:127], v[82:97]
	ds_read_b128 v[144:147], v155
	ds_read_b128 v[132:135], v153
	v_mfma_f32_32x32x16_f16 v[34:49], v[112:115], v[128:131], v[34:49]
	ds_read_b128 v[148:151], v155 offset:2048
	ds_read_b128 v[136:139], v153 offset:2048
	v_mfma_f32_32x32x16_f16 v[66:81], v[116:119], v[124:127], v[66:81]
	ds_read_b128 v[140:143], v153 offset:4096
	v_mfma_f32_32x32x16_f16 v[18:33], v[116:119], v[128:131], v[18:33]
	v_mfma_f32_32x32x16_f16 v[50:65], v[120:123], v[124:127], v[50:65]
	v_mfma_f32_32x32x16_f16 v[2:17], v[120:123], v[128:131], v[2:17]
	s_waitcnt lgkmcnt(0)
	s_barrier
	v_mfma_f32_32x32x16_f16 v[82:97], v[132:135], v[144:147], v[82:97]
	ds_read_b128 v[124:127], v103
	ds_read_b128 v[112:115], v101
	v_mfma_f32_32x32x16_f16 v[34:49], v[132:135], v[148:151], v[34:49]
	ds_read_b128 v[128:131], v103 offset:2048
	ds_read_b128 v[116:119], v101 offset:2048
	v_mfma_f32_32x32x16_f16 v[66:81], v[136:139], v[144:147], v[66:81]
	ds_read_b128 v[120:123], v101 offset:4096
	v_mfma_f32_32x32x16_f16 v[18:33], v[136:139], v[148:151], v[18:33]
	v_mfma_f32_32x32x16_f16 v[50:65], v[140:143], v[144:147], v[50:65]
	v_mfma_f32_32x32x16_f16 v[2:17], v[140:143], v[148:151], v[2:17]
	s_waitcnt lgkmcnt(0)
	v_mfma_f32_32x32x16_f16 v[82:97], v[112:115], v[124:127], v[82:97]
	ds_read_b128 v[144:147], v104
	ds_read_b128 v[132:135], v102
	v_mfma_f32_32x32x16_f16 v[34:49], v[112:115], v[128:131], v[34:49]
	ds_read_b128 v[148:151], v104 offset:2048
	ds_read_b128 v[136:139], v102 offset:2048
	v_mfma_f32_32x32x16_f16 v[66:81], v[116:119], v[124:127], v[66:81]
	ds_read_b128 v[140:143], v102 offset:4096
	v_mfma_f32_32x32x16_f16 v[18:33], v[116:119], v[128:131], v[18:33]
	v_mfma_f32_32x32x16_f16 v[50:65], v[120:123], v[124:127], v[50:65]
	v_mfma_f32_32x32x16_f16 v[2:17], v[120:123], v[128:131], v[2:17]
	s_waitcnt lgkmcnt(0)
	s_barrier
	v_mfma_f32_32x32x16_f16 v[82:97], v[132:135], v[144:147], v[82:97]
	ds_read_b128 v[124:127], v103 offset:28672
	ds_read_b128 v[112:115], v101 offset:28672
	v_mfma_f32_32x32x16_f16 v[34:49], v[132:135], v[148:151], v[34:49]
	ds_read_b128 v[128:131], v103 offset:30720
	ds_read_b128 v[116:119], v101 offset:30720
	v_mfma_f32_32x32x16_f16 v[66:81], v[136:139], v[144:147], v[66:81]
	ds_read_b128 v[120:123], v101 offset:32768
	v_mfma_f32_32x32x16_f16 v[18:33], v[136:139], v[148:151], v[18:33]
	v_mfma_f32_32x32x16_f16 v[50:65], v[140:143], v[144:147], v[50:65]
	v_mfma_f32_32x32x16_f16 v[2:17], v[140:143], v[148:151], v[2:17]
	s_waitcnt lgkmcnt(0)
	v_mfma_f32_32x32x16_f16 v[82:97], v[112:115], v[124:127], v[82:97]
	ds_read_b128 v[144:147], v104 offset:28672
	ds_read_b128 v[132:135], v102 offset:28672
	v_mfma_f32_32x32x16_f16 v[34:49], v[112:115], v[128:131], v[34:49]
	ds_read_b128 v[148:151], v104 offset:30720
	ds_read_b128 v[136:139], v102 offset:30720
	v_mfma_f32_32x32x16_f16 v[66:81], v[116:119], v[124:127], v[66:81]
	ds_read_b128 v[140:143], v102 offset:32768
	v_mfma_f32_32x32x16_f16 v[18:33], v[116:119], v[128:131], v[18:33]
	v_mfma_f32_32x32x16_f16 v[50:65], v[120:123], v[124:127], v[50:65]
	v_mfma_f32_32x32x16_f16 v[2:17], v[120:123], v[128:131], v[2:17]
	s_waitcnt lgkmcnt(0)
	s_barrier
	v_mfma_f32_32x32x16_f16 v[82:97], v[132:135], v[144:147], v[82:97]
	ds_read_b128 v[124:127], v107
	ds_read_b128 v[112:115], v105
	v_mfma_f32_32x32x16_f16 v[34:49], v[132:135], v[148:151], v[34:49]
	ds_read_b128 v[128:131], v107 offset:2048
	ds_read_b128 v[116:119], v105 offset:2048
	v_mfma_f32_32x32x16_f16 v[66:81], v[136:139], v[144:147], v[66:81]
	ds_read_b128 v[120:123], v105 offset:4096
	v_mfma_f32_32x32x16_f16 v[18:33], v[136:139], v[148:151], v[18:33]
	v_mfma_f32_32x32x16_f16 v[50:65], v[140:143], v[144:147], v[50:65]
	v_mfma_f32_32x32x16_f16 v[2:17], v[140:143], v[148:151], v[2:17]
	s_waitcnt lgkmcnt(0)
	v_mfma_f32_32x32x16_f16 v[82:97], v[112:115], v[124:127], v[82:97]
	ds_read_b128 v[144:147], v108
	ds_read_b128 v[132:135], v106
	v_mfma_f32_32x32x16_f16 v[34:49], v[112:115], v[128:131], v[34:49]
	ds_read_b128 v[148:151], v108 offset:2048
	ds_read_b128 v[136:139], v106 offset:2048
	v_mfma_f32_32x32x16_f16 v[66:81], v[116:119], v[124:127], v[66:81]
	ds_read_b128 v[140:143], v106 offset:4096
	v_mfma_f32_32x32x16_f16 v[18:33], v[116:119], v[128:131], v[18:33]
	v_mfma_f32_32x32x16_f16 v[50:65], v[120:123], v[124:127], v[50:65]
	v_mfma_f32_32x32x16_f16 v[2:17], v[120:123], v[128:131], v[2:17]
	s_waitcnt lgkmcnt(0)
	s_barrier
	v_mfma_f32_32x32x16_f16 v[82:97], v[132:135], v[144:147], v[82:97]
	ds_read_b128 v[124:127], v107 offset:28672
	ds_read_b128 v[112:115], v105 offset:28672
	v_mfma_f32_32x32x16_f16 v[34:49], v[132:135], v[148:151], v[34:49]
	ds_read_b128 v[128:131], v107 offset:30720
	ds_read_b128 v[116:119], v105 offset:30720
	v_mfma_f32_32x32x16_f16 v[66:81], v[136:139], v[144:147], v[66:81]
	ds_read_b128 v[120:123], v105 offset:32768
	v_mfma_f32_32x32x16_f16 v[18:33], v[136:139], v[148:151], v[18:33]
	v_mfma_f32_32x32x16_f16 v[50:65], v[140:143], v[144:147], v[50:65]
	v_mfma_f32_32x32x16_f16 v[2:17], v[140:143], v[148:151], v[2:17]
	s_waitcnt lgkmcnt(0)
	v_mfma_f32_32x32x16_f16 v[82:97], v[112:115], v[124:127], v[82:97]
	ds_read_b128 v[144:147], v108 offset:28672
	ds_read_b128 v[132:135], v106 offset:28672
	v_mfma_f32_32x32x16_f16 v[34:49], v[112:115], v[128:131], v[34:49]
	ds_read_b128 v[148:151], v108 offset:30720
	ds_read_b128 v[136:139], v106 offset:30720
	v_mfma_f32_32x32x16_f16 v[66:81], v[116:119], v[124:127], v[66:81]
	ds_read_b128 v[140:143], v106 offset:32768
	v_mfma_f32_32x32x16_f16 v[18:33], v[116:119], v[128:131], v[18:33]
	v_mfma_f32_32x32x16_f16 v[50:65], v[120:123], v[124:127], v[50:65]
	v_mfma_f32_32x32x16_f16 v[2:17], v[120:123], v[128:131], v[2:17]
	s_waitcnt lgkmcnt(0)
	s_barrier
	v_mfma_f32_32x32x16_f16 v[82:97], v[132:135], v[144:147], v[82:97]
	ds_read_b128 v[124:127], v154
	ds_read_b128 v[112:115], v152
	v_mfma_f32_32x32x16_f16 v[34:49], v[132:135], v[148:151], v[34:49]
	ds_read_b128 v[128:131], v154 offset:2048
	ds_read_b128 v[116:119], v152 offset:2048
	v_mfma_f32_32x32x16_f16 v[66:81], v[136:139], v[144:147], v[66:81]
	ds_read_b128 v[120:123], v152 offset:4096
	v_mfma_f32_32x32x16_f16 v[18:33], v[136:139], v[148:151], v[18:33]
	v_mfma_f32_32x32x16_f16 v[50:65], v[140:143], v[144:147], v[50:65]
	v_mfma_f32_32x32x16_f16 v[2:17], v[140:143], v[148:151], v[2:17]
	s_waitcnt lgkmcnt(0)
	v_mfma_f32_32x32x16_f16 v[82:97], v[112:115], v[124:127], v[82:97]
	ds_read_b128 v[144:147], v155
	ds_read_b128 v[132:135], v153
	v_mfma_f32_32x32x16_f16 v[34:49], v[112:115], v[128:131], v[34:49]
	ds_read_b128 v[148:151], v155 offset:2048
	ds_read_b128 v[136:139], v153 offset:2048
	v_mfma_f32_32x32x16_f16 v[66:81], v[116:119], v[124:127], v[66:81]
	ds_read_b128 v[140:143], v153 offset:4096
	v_mfma_f32_32x32x16_f16 v[18:33], v[116:119], v[128:131], v[18:33]
	v_mfma_f32_32x32x16_f16 v[50:65], v[120:123], v[124:127], v[50:65]
	v_mfma_f32_32x32x16_f16 v[2:17], v[120:123], v[128:131], v[2:17]
	s_waitcnt lgkmcnt(0)
	s_barrier
	v_mfma_f32_32x32x16_f16 v[82:97], v[132:135], v[144:147], v[82:97]
	ds_read_b128 v[124:127], v103
	ds_read_b128 v[112:115], v101
	v_mfma_f32_32x32x16_f16 v[34:49], v[132:135], v[148:151], v[34:49]
	ds_read_b128 v[128:131], v103 offset:2048
	ds_read_b128 v[116:119], v101 offset:2048
	v_mfma_f32_32x32x16_f16 v[66:81], v[136:139], v[144:147], v[66:81]
	ds_read_b128 v[120:123], v101 offset:4096
	v_mfma_f32_32x32x16_f16 v[18:33], v[136:139], v[148:151], v[18:33]
	v_mfma_f32_32x32x16_f16 v[50:65], v[140:143], v[144:147], v[50:65]
	v_mfma_f32_32x32x16_f16 v[2:17], v[140:143], v[148:151], v[2:17]
	s_waitcnt lgkmcnt(0)
	v_mfma_f32_32x32x16_f16 v[82:97], v[112:115], v[124:127], v[82:97]
	ds_read_b128 v[144:147], v104
	ds_read_b128 v[132:135], v102
	v_mfma_f32_32x32x16_f16 v[34:49], v[112:115], v[128:131], v[34:49]
	ds_read_b128 v[148:151], v104 offset:2048
	ds_read_b128 v[136:139], v102 offset:2048
	v_mfma_f32_32x32x16_f16 v[66:81], v[116:119], v[124:127], v[66:81]
	ds_read_b128 v[140:143], v102 offset:4096
	v_mfma_f32_32x32x16_f16 v[18:33], v[116:119], v[128:131], v[18:33]
	v_mfma_f32_32x32x16_f16 v[50:65], v[120:123], v[124:127], v[50:65]
	v_mfma_f32_32x32x16_f16 v[2:17], v[120:123], v[128:131], v[2:17]
	s_waitcnt lgkmcnt(0)
	s_barrier
	v_mfma_f32_32x32x16_f16 v[82:97], v[132:135], v[144:147], v[82:97]
	ds_read_b128 v[124:127], v103 offset:28672
	ds_read_b128 v[112:115], v101 offset:28672
	v_mfma_f32_32x32x16_f16 v[34:49], v[132:135], v[148:151], v[34:49]
	ds_read_b128 v[128:131], v103 offset:30720
	ds_read_b128 v[116:119], v101 offset:30720
	v_mfma_f32_32x32x16_f16 v[66:81], v[136:139], v[144:147], v[66:81]
	ds_read_b128 v[120:123], v101 offset:32768
	v_mfma_f32_32x32x16_f16 v[18:33], v[136:139], v[148:151], v[18:33]
	v_mfma_f32_32x32x16_f16 v[50:65], v[140:143], v[144:147], v[50:65]
	v_mfma_f32_32x32x16_f16 v[2:17], v[140:143], v[148:151], v[2:17]
	s_waitcnt lgkmcnt(0)
	v_mfma_f32_32x32x16_f16 v[82:97], v[112:115], v[124:127], v[82:97]
	ds_read_b128 v[144:147], v104 offset:28672
	ds_read_b128 v[132:135], v102 offset:28672
	v_mfma_f32_32x32x16_f16 v[34:49], v[112:115], v[128:131], v[34:49]
	ds_read_b128 v[148:151], v104 offset:30720
	ds_read_b128 v[136:139], v102 offset:30720
	v_mfma_f32_32x32x16_f16 v[66:81], v[116:119], v[124:127], v[66:81]
	ds_read_b128 v[140:143], v102 offset:32768
	v_mfma_f32_32x32x16_f16 v[18:33], v[116:119], v[128:131], v[18:33]
	v_mfma_f32_32x32x16_f16 v[50:65], v[120:123], v[124:127], v[50:65]
	v_mfma_f32_32x32x16_f16 v[2:17], v[120:123], v[128:131], v[2:17]
	s_waitcnt lgkmcnt(0)
	s_barrier
	v_mfma_f32_32x32x16_f16 v[82:97], v[132:135], v[144:147], v[82:97]
	ds_read_b128 v[124:127], v107
	ds_read_b128 v[112:115], v105
	v_mfma_f32_32x32x16_f16 v[34:49], v[132:135], v[148:151], v[34:49]
	ds_read_b128 v[128:131], v107 offset:2048
	ds_read_b128 v[116:119], v105 offset:2048
	v_mfma_f32_32x32x16_f16 v[66:81], v[136:139], v[144:147], v[66:81]
	ds_read_b128 v[120:123], v105 offset:4096
	v_mfma_f32_32x32x16_f16 v[18:33], v[136:139], v[148:151], v[18:33]
	v_mfma_f32_32x32x16_f16 v[50:65], v[140:143], v[144:147], v[50:65]
	v_mfma_f32_32x32x16_f16 v[2:17], v[140:143], v[148:151], v[2:17]
	s_waitcnt lgkmcnt(0)
	v_mfma_f32_32x32x16_f16 v[82:97], v[112:115], v[124:127], v[82:97]
	ds_read_b128 v[144:147], v108
	ds_read_b128 v[132:135], v106
	v_mfma_f32_32x32x16_f16 v[34:49], v[112:115], v[128:131], v[34:49]
	ds_read_b128 v[148:151], v108 offset:2048
	ds_read_b128 v[136:139], v106 offset:2048
	v_mfma_f32_32x32x16_f16 v[66:81], v[116:119], v[124:127], v[66:81]
	ds_read_b128 v[140:143], v106 offset:4096
	v_mfma_f32_32x32x16_f16 v[18:33], v[116:119], v[128:131], v[18:33]
	v_mfma_f32_32x32x16_f16 v[50:65], v[120:123], v[124:127], v[50:65]
	v_mfma_f32_32x32x16_f16 v[2:17], v[120:123], v[128:131], v[2:17]
	s_waitcnt lgkmcnt(0)
	s_barrier
	v_mfma_f32_32x32x16_f16 v[82:97], v[132:135], v[144:147], v[82:97]
	ds_read_b128 v[124:127], v107 offset:28672
	ds_read_b128 v[112:115], v105 offset:28672
	v_mfma_f32_32x32x16_f16 v[34:49], v[132:135], v[148:151], v[34:49]
	ds_read_b128 v[128:131], v107 offset:30720
	ds_read_b128 v[116:119], v105 offset:30720
	v_mfma_f32_32x32x16_f16 v[66:81], v[136:139], v[144:147], v[66:81]
	ds_read_b128 v[120:123], v105 offset:32768
	v_mfma_f32_32x32x16_f16 v[18:33], v[136:139], v[148:151], v[18:33]
	v_mfma_f32_32x32x16_f16 v[50:65], v[140:143], v[144:147], v[50:65]
	v_mfma_f32_32x32x16_f16 v[2:17], v[140:143], v[148:151], v[2:17]
	s_waitcnt lgkmcnt(0)
	v_mfma_f32_32x32x16_f16 v[82:97], v[112:115], v[124:127], v[82:97]
	ds_read_b128 v[144:147], v108 offset:28672
	ds_read_b128 v[132:135], v106 offset:28672
	v_mfma_f32_32x32x16_f16 v[34:49], v[112:115], v[128:131], v[34:49]
	ds_read_b128 v[148:151], v108 offset:30720
	ds_read_b128 v[136:139], v106 offset:30720
	v_mfma_f32_32x32x16_f16 v[66:81], v[116:119], v[124:127], v[66:81]
	ds_read_b128 v[140:143], v106 offset:32768
	v_mfma_f32_32x32x16_f16 v[18:33], v[116:119], v[128:131], v[18:33]
	v_mfma_f32_32x32x16_f16 v[50:65], v[120:123], v[124:127], v[50:65]
	v_mfma_f32_32x32x16_f16 v[2:17], v[120:123], v[128:131], v[2:17]
	s_waitcnt lgkmcnt(0)
	s_barrier
	v_mfma_f32_32x32x16_f16 v[82:97], v[132:135], v[144:147], v[82:97]
	ds_read_b128 v[124:127], v154
	ds_read_b128 v[112:115], v152
	v_mfma_f32_32x32x16_f16 v[34:49], v[132:135], v[148:151], v[34:49]
	ds_read_b128 v[128:131], v154 offset:2048
	ds_read_b128 v[116:119], v152 offset:2048
	v_mfma_f32_32x32x16_f16 v[66:81], v[136:139], v[144:147], v[66:81]
	ds_read_b128 v[120:123], v152 offset:4096
	v_mfma_f32_32x32x16_f16 v[18:33], v[136:139], v[148:151], v[18:33]
	v_mfma_f32_32x32x16_f16 v[50:65], v[140:143], v[144:147], v[50:65]
	v_mfma_f32_32x32x16_f16 v[2:17], v[140:143], v[148:151], v[2:17]
	s_waitcnt lgkmcnt(0)
	v_mfma_f32_32x32x16_f16 v[82:97], v[112:115], v[124:127], v[82:97]
	ds_read_b128 v[144:147], v155
	ds_read_b128 v[132:135], v153
	v_mfma_f32_32x32x16_f16 v[34:49], v[112:115], v[128:131], v[34:49]
	ds_read_b128 v[148:151], v155 offset:2048
	ds_read_b128 v[136:139], v153 offset:2048
	v_mfma_f32_32x32x16_f16 v[66:81], v[116:119], v[124:127], v[66:81]
	ds_read_b128 v[140:143], v153 offset:4096
	v_mfma_f32_32x32x16_f16 v[18:33], v[116:119], v[128:131], v[18:33]
	v_mfma_f32_32x32x16_f16 v[50:65], v[120:123], v[124:127], v[50:65]
	v_mfma_f32_32x32x16_f16 v[2:17], v[120:123], v[128:131], v[2:17]
	s_waitcnt lgkmcnt(0)
	s_barrier
	v_mfma_f32_32x32x16_f16 v[82:97], v[132:135], v[144:147], v[82:97]
	ds_read_b128 v[124:127], v103
	ds_read_b128 v[112:115], v101
	v_mfma_f32_32x32x16_f16 v[34:49], v[132:135], v[148:151], v[34:49]
	ds_read_b128 v[128:131], v103 offset:2048
	ds_read_b128 v[116:119], v101 offset:2048
	v_mfma_f32_32x32x16_f16 v[66:81], v[136:139], v[144:147], v[66:81]
	ds_read_b128 v[120:123], v101 offset:4096
	v_mfma_f32_32x32x16_f16 v[18:33], v[136:139], v[148:151], v[18:33]
	v_mfma_f32_32x32x16_f16 v[50:65], v[140:143], v[144:147], v[50:65]
	v_mfma_f32_32x32x16_f16 v[2:17], v[140:143], v[148:151], v[2:17]
	s_waitcnt lgkmcnt(0)
	v_mfma_f32_32x32x16_f16 v[82:97], v[112:115], v[124:127], v[82:97]
	ds_read_b128 v[144:147], v104
	ds_read_b128 v[132:135], v102
	v_mfma_f32_32x32x16_f16 v[34:49], v[112:115], v[128:131], v[34:49]
	ds_read_b128 v[148:151], v104 offset:2048
	ds_read_b128 v[136:139], v102 offset:2048
	v_mfma_f32_32x32x16_f16 v[66:81], v[116:119], v[124:127], v[66:81]
	ds_read_b128 v[140:143], v102 offset:4096
	v_mfma_f32_32x32x16_f16 v[18:33], v[116:119], v[128:131], v[18:33]
	v_mfma_f32_32x32x16_f16 v[50:65], v[120:123], v[124:127], v[50:65]
	v_mfma_f32_32x32x16_f16 v[2:17], v[120:123], v[128:131], v[2:17]
	s_waitcnt lgkmcnt(0)
	s_barrier
	v_mfma_f32_32x32x16_f16 v[82:97], v[132:135], v[144:147], v[82:97]
	ds_read_b128 v[124:127], v103 offset:28672
	ds_read_b128 v[112:115], v101 offset:28672
	v_mfma_f32_32x32x16_f16 v[34:49], v[132:135], v[148:151], v[34:49]
	ds_read_b128 v[128:131], v103 offset:30720
	ds_read_b128 v[116:119], v101 offset:30720
	v_mfma_f32_32x32x16_f16 v[66:81], v[136:139], v[144:147], v[66:81]
	ds_read_b128 v[120:123], v101 offset:32768
	v_mfma_f32_32x32x16_f16 v[18:33], v[136:139], v[148:151], v[18:33]
	v_mfma_f32_32x32x16_f16 v[50:65], v[140:143], v[144:147], v[50:65]
	v_mfma_f32_32x32x16_f16 v[2:17], v[140:143], v[148:151], v[2:17]
	s_waitcnt lgkmcnt(0)
	v_mfma_f32_32x32x16_f16 v[82:97], v[112:115], v[124:127], v[82:97]
	ds_read_b128 v[144:147], v104 offset:28672
	ds_read_b128 v[132:135], v102 offset:28672
	v_mfma_f32_32x32x16_f16 v[34:49], v[112:115], v[128:131], v[34:49]
	ds_read_b128 v[148:151], v104 offset:30720
	ds_read_b128 v[136:139], v102 offset:30720
	v_mfma_f32_32x32x16_f16 v[66:81], v[116:119], v[124:127], v[66:81]
	ds_read_b128 v[140:143], v102 offset:32768
	v_mfma_f32_32x32x16_f16 v[18:33], v[116:119], v[128:131], v[18:33]
	v_mfma_f32_32x32x16_f16 v[50:65], v[120:123], v[124:127], v[50:65]
	v_mfma_f32_32x32x16_f16 v[2:17], v[120:123], v[128:131], v[2:17]
	s_waitcnt lgkmcnt(0)
	s_barrier
	v_mfma_f32_32x32x16_f16 v[82:97], v[132:135], v[144:147], v[82:97]
	ds_read_b128 v[124:127], v107
	ds_read_b128 v[112:115], v105
	v_mfma_f32_32x32x16_f16 v[34:49], v[132:135], v[148:151], v[34:49]
	ds_read_b128 v[128:131], v107 offset:2048
	ds_read_b128 v[116:119], v105 offset:2048
	v_mfma_f32_32x32x16_f16 v[66:81], v[136:139], v[144:147], v[66:81]
	ds_read_b128 v[120:123], v105 offset:4096
	v_mfma_f32_32x32x16_f16 v[18:33], v[136:139], v[148:151], v[18:33]
	v_mfma_f32_32x32x16_f16 v[50:65], v[140:143], v[144:147], v[50:65]
	v_mfma_f32_32x32x16_f16 v[2:17], v[140:143], v[148:151], v[2:17]
	s_waitcnt lgkmcnt(0)
	v_mfma_f32_32x32x16_f16 v[82:97], v[112:115], v[124:127], v[82:97]
	ds_read_b128 v[144:147], v108
	ds_read_b128 v[132:135], v106
	v_mfma_f32_32x32x16_f16 v[34:49], v[112:115], v[128:131], v[34:49]
	ds_read_b128 v[148:151], v108 offset:2048
	ds_read_b128 v[136:139], v106 offset:2048
	v_mfma_f32_32x32x16_f16 v[66:81], v[116:119], v[124:127], v[66:81]
	ds_read_b128 v[140:143], v106 offset:4096
	v_mfma_f32_32x32x16_f16 v[18:33], v[116:119], v[128:131], v[18:33]
	v_mfma_f32_32x32x16_f16 v[50:65], v[120:123], v[124:127], v[50:65]
	v_mfma_f32_32x32x16_f16 v[2:17], v[120:123], v[128:131], v[2:17]
	s_waitcnt lgkmcnt(0)
	s_barrier
	v_mfma_f32_32x32x16_f16 v[82:97], v[132:135], v[144:147], v[82:97]
	ds_read_b128 v[124:127], v107 offset:28672
	ds_read_b128 v[112:115], v105 offset:28672
	v_mfma_f32_32x32x16_f16 v[34:49], v[132:135], v[148:151], v[34:49]
	ds_read_b128 v[128:131], v107 offset:30720
	ds_read_b128 v[116:119], v105 offset:30720
	v_mfma_f32_32x32x16_f16 v[66:81], v[136:139], v[144:147], v[66:81]
	ds_read_b128 v[120:123], v105 offset:32768
	v_mfma_f32_32x32x16_f16 v[18:33], v[136:139], v[148:151], v[18:33]
	v_mfma_f32_32x32x16_f16 v[50:65], v[140:143], v[144:147], v[50:65]
	v_mfma_f32_32x32x16_f16 v[2:17], v[140:143], v[148:151], v[2:17]
	s_waitcnt lgkmcnt(0)
	v_mfma_f32_32x32x16_f16 v[82:97], v[112:115], v[124:127], v[82:97]
	ds_read_b128 v[144:147], v108 offset:28672
	ds_read_b128 v[132:135], v106 offset:28672
	v_mfma_f32_32x32x16_f16 v[34:49], v[112:115], v[128:131], v[34:49]
	ds_read_b128 v[148:151], v108 offset:30720
	ds_read_b128 v[136:139], v106 offset:30720
	v_mfma_f32_32x32x16_f16 v[66:81], v[116:119], v[124:127], v[66:81]
	ds_read_b128 v[140:143], v106 offset:32768
	v_mfma_f32_32x32x16_f16 v[18:33], v[116:119], v[128:131], v[18:33]
	v_mfma_f32_32x32x16_f16 v[50:65], v[120:123], v[124:127], v[50:65]
	v_mfma_f32_32x32x16_f16 v[2:17], v[120:123], v[128:131], v[2:17]
	s_waitcnt lgkmcnt(0)
	v_mfma_f32_32x32x16_f16 v[82:97], v[132:135], v[144:147], v[82:97]
	v_mfma_f32_32x32x16_f16 v[34:49], v[132:135], v[148:151], v[34:49]
	v_mfma_f32_32x32x16_f16 v[66:81], v[136:139], v[144:147], v[66:81]
	v_mfma_f32_32x32x16_f16 v[18:33], v[136:139], v[148:151], v[18:33]
	v_mfma_f32_32x32x16_f16 v[50:65], v[140:143], v[144:147], v[50:65]
	v_mfma_f32_32x32x16_f16 v[2:17], v[140:143], v[148:151], v[2:17]
	s_branch .LBB1_35
.Lqkv_cv:
	s_barrier
	ds_read_b128 v[124:127], v103
	ds_read_b128 v[112:115], v101
	ds_read_b128 v[128:131], v103 offset:2048
	ds_read_b128 v[116:119], v101 offset:2048
	ds_read_b128 v[120:123], v101 offset:4096
	s_waitcnt lgkmcnt(0)
	v_mfma_f32_32x32x16_f16 v[82:97], v[124:127], v[112:115], v[82:97]
	ds_read_b128 v[144:147], v104
	ds_read_b128 v[132:135], v102
	v_mfma_f32_32x32x16_f16 v[34:49], v[128:131], v[112:115], v[34:49]
	ds_read_b128 v[148:151], v104 offset:2048
	ds_read_b128 v[136:139], v102 offset:2048
	v_mfma_f32_32x32x16_f16 v[66:81], v[124:127], v[116:119], v[66:81]
	ds_read_b128 v[140:143], v102 offset:4096
	v_mfma_f32_32x32x16_f16 v[18:33], v[128:131], v[116:119], v[18:33]
	v_mfma_f32_32x32x16_f16 v[50:65], v[124:127], v[120:123], v[50:65]
	v_mfma_f32_32x32x16_f16 v[2:17], v[128:131], v[120:123], v[2:17]
	s_waitcnt lgkmcnt(0)
	s_barrier
	v_mfma_f32_32x32x16_f16 v[82:97], v[144:147], v[132:135], v[82:97]
	ds_read_b128 v[124:127], v103 offset:28672
	ds_read_b128 v[112:115], v101 offset:28672
	v_mfma_f32_32x32x16_f16 v[34:49], v[148:151], v[132:135], v[34:49]
	ds_read_b128 v[128:131], v103 offset:30720
	ds_read_b128 v[116:119], v101 offset:30720
	v_mfma_f32_32x32x16_f16 v[66:81], v[144:147], v[136:139], v[66:81]
	ds_read_b128 v[120:123], v101 offset:32768
	v_mfma_f32_32x32x16_f16 v[18:33], v[148:151], v[136:139], v[18:33]
	v_mfma_f32_32x32x16_f16 v[50:65], v[144:147], v[140:143], v[50:65]
	v_mfma_f32_32x32x16_f16 v[2:17], v[148:151], v[140:143], v[2:17]
	s_waitcnt lgkmcnt(0)
	v_mfma_f32_32x32x16_f16 v[82:97], v[124:127], v[112:115], v[82:97]
	ds_read_b128 v[144:147], v104 offset:28672
	ds_read_b128 v[132:135], v102 offset:28672
	v_mfma_f32_32x32x16_f16 v[34:49], v[128:131], v[112:115], v[34:49]
	ds_read_b128 v[148:151], v104 offset:30720
	ds_read_b128 v[136:139], v102 offset:30720
	v_mfma_f32_32x32x16_f16 v[66:81], v[124:127], v[116:119], v[66:81]
	ds_read_b128 v[140:143], v102 offset:32768
	v_mfma_f32_32x32x16_f16 v[18:33], v[128:131], v[116:119], v[18:33]
	v_mfma_f32_32x32x16_f16 v[50:65], v[124:127], v[120:123], v[50:65]
	v_mfma_f32_32x32x16_f16 v[2:17], v[128:131], v[120:123], v[2:17]
	s_waitcnt lgkmcnt(0)
	s_barrier
	v_mfma_f32_32x32x16_f16 v[82:97], v[144:147], v[132:135], v[82:97]
	ds_read_b128 v[124:127], v107
	ds_read_b128 v[112:115], v105
	v_mfma_f32_32x32x16_f16 v[34:49], v[148:151], v[132:135], v[34:49]
	ds_read_b128 v[128:131], v107 offset:2048
	ds_read_b128 v[116:119], v105 offset:2048
	v_mfma_f32_32x32x16_f16 v[66:81], v[144:147], v[136:139], v[66:81]
	ds_read_b128 v[120:123], v105 offset:4096
	v_mfma_f32_32x32x16_f16 v[18:33], v[148:151], v[136:139], v[18:33]
	v_mfma_f32_32x32x16_f16 v[50:65], v[144:147], v[140:143], v[50:65]
	v_mfma_f32_32x32x16_f16 v[2:17], v[148:151], v[140:143], v[2:17]
	s_waitcnt lgkmcnt(0)
	v_mfma_f32_32x32x16_f16 v[82:97], v[124:127], v[112:115], v[82:97]
	ds_read_b128 v[144:147], v108
	ds_read_b128 v[132:135], v106
	v_mfma_f32_32x32x16_f16 v[34:49], v[128:131], v[112:115], v[34:49]
	ds_read_b128 v[148:151], v108 offset:2048
	ds_read_b128 v[136:139], v106 offset:2048
	v_mfma_f32_32x32x16_f16 v[66:81], v[124:127], v[116:119], v[66:81]
	ds_read_b128 v[140:143], v106 offset:4096
	v_mfma_f32_32x32x16_f16 v[18:33], v[128:131], v[116:119], v[18:33]
	v_mfma_f32_32x32x16_f16 v[50:65], v[124:127], v[120:123], v[50:65]
	v_mfma_f32_32x32x16_f16 v[2:17], v[128:131], v[120:123], v[2:17]
	s_waitcnt lgkmcnt(0)
	s_barrier
	v_mfma_f32_32x32x16_f16 v[82:97], v[144:147], v[132:135], v[82:97]
	ds_read_b128 v[124:127], v107 offset:28672
	ds_read_b128 v[112:115], v105 offset:28672
	v_mfma_f32_32x32x16_f16 v[34:49], v[148:151], v[132:135], v[34:49]
	ds_read_b128 v[128:131], v107 offset:30720
	ds_read_b128 v[116:119], v105 offset:30720
	v_mfma_f32_32x32x16_f16 v[66:81], v[144:147], v[136:139], v[66:81]
	ds_read_b128 v[120:123], v105 offset:32768
	v_mfma_f32_32x32x16_f16 v[18:33], v[148:151], v[136:139], v[18:33]
	v_mfma_f32_32x32x16_f16 v[50:65], v[144:147], v[140:143], v[50:65]
	v_mfma_f32_32x32x16_f16 v[2:17], v[148:151], v[140:143], v[2:17]
	s_waitcnt lgkmcnt(0)
	v_mfma_f32_32x32x16_f16 v[82:97], v[124:127], v[112:115], v[82:97]
	ds_read_b128 v[144:147], v108 offset:28672
	ds_read_b128 v[132:135], v106 offset:28672
	v_mfma_f32_32x32x16_f16 v[34:49], v[128:131], v[112:115], v[34:49]
	ds_read_b128 v[148:151], v108 offset:30720
	ds_read_b128 v[136:139], v106 offset:30720
	v_mfma_f32_32x32x16_f16 v[66:81], v[124:127], v[116:119], v[66:81]
	ds_read_b128 v[140:143], v106 offset:32768
	v_mfma_f32_32x32x16_f16 v[18:33], v[128:131], v[116:119], v[18:33]
	v_mfma_f32_32x32x16_f16 v[50:65], v[124:127], v[120:123], v[50:65]
	v_mfma_f32_32x32x16_f16 v[2:17], v[128:131], v[120:123], v[2:17]
	s_waitcnt lgkmcnt(0)
	s_barrier
	v_mfma_f32_32x32x16_f16 v[82:97], v[144:147], v[132:135], v[82:97]
	ds_read_b128 v[124:127], v154
	ds_read_b128 v[112:115], v152
	v_mfma_f32_32x32x16_f16 v[34:49], v[148:151], v[132:135], v[34:49]
	ds_read_b128 v[128:131], v154 offset:2048
	ds_read_b128 v[116:119], v152 offset:2048
	v_mfma_f32_32x32x16_f16 v[66:81], v[144:147], v[136:139], v[66:81]
	ds_read_b128 v[120:123], v152 offset:4096
	v_mfma_f32_32x32x16_f16 v[18:33], v[148:151], v[136:139], v[18:33]
	v_mfma_f32_32x32x16_f16 v[50:65], v[144:147], v[140:143], v[50:65]
	v_mfma_f32_32x32x16_f16 v[2:17], v[148:151], v[140:143], v[2:17]
	s_waitcnt lgkmcnt(0)
	v_mfma_f32_32x32x16_f16 v[82:97], v[124:127], v[112:115], v[82:97]
	ds_read_b128 v[144:147], v155
	ds_read_b128 v[132:135], v153
	v_mfma_f32_32x32x16_f16 v[34:49], v[128:131], v[112:115], v[34:49]
	ds_read_b128 v[148:151], v155 offset:2048
	ds_read_b128 v[136:139], v153 offset:2048
	v_mfma_f32_32x32x16_f16 v[66:81], v[124:127], v[116:119], v[66:81]
	ds_read_b128 v[140:143], v153 offset:4096
	v_mfma_f32_32x32x16_f16 v[18:33], v[128:131], v[116:119], v[18:33]
	v_mfma_f32_32x32x16_f16 v[50:65], v[124:127], v[120:123], v[50:65]
	v_mfma_f32_32x32x16_f16 v[2:17], v[128:131], v[120:123], v[2:17]
	s_waitcnt lgkmcnt(0)
	s_barrier
	v_mfma_f32_32x32x16_f16 v[82:97], v[144:147], v[132:135], v[82:97]
	ds_read_b128 v[124:127], v103
	ds_read_b128 v[112:115], v101
	v_mfma_f32_32x32x16_f16 v[34:49], v[148:151], v[132:135], v[34:49]
	ds_read_b128 v[128:131], v103 offset:2048
	ds_read_b128 v[116:119], v101 offset:2048
	v_mfma_f32_32x32x16_f16 v[66:81], v[144:147], v[136:139], v[66:81]
	ds_read_b128 v[120:123], v101 offset:4096
	v_mfma_f32_32x32x16_f16 v[18:33], v[148:151], v[136:139], v[18:33]
	v_mfma_f32_32x32x16_f16 v[50:65], v[144:147], v[140:143], v[50:65]
	v_mfma_f32_32x32x16_f16 v[2:17], v[148:151], v[140:143], v[2:17]
	s_waitcnt lgkmcnt(0)
	v_mfma_f32_32x32x16_f16 v[82:97], v[124:127], v[112:115], v[82:97]
	ds_read_b128 v[144:147], v104
	ds_read_b128 v[132:135], v102
	v_mfma_f32_32x32x16_f16 v[34:49], v[128:131], v[112:115], v[34:49]
	ds_read_b128 v[148:151], v104 offset:2048
	ds_read_b128 v[136:139], v102 offset:2048
	v_mfma_f32_32x32x16_f16 v[66:81], v[124:127], v[116:119], v[66:81]
	ds_read_b128 v[140:143], v102 offset:4096
	v_mfma_f32_32x32x16_f16 v[18:33], v[128:131], v[116:119], v[18:33]
	v_mfma_f32_32x32x16_f16 v[50:65], v[124:127], v[120:123], v[50:65]
	v_mfma_f32_32x32x16_f16 v[2:17], v[128:131], v[120:123], v[2:17]
	s_waitcnt lgkmcnt(0)
	s_barrier
	v_mfma_f32_32x32x16_f16 v[82:97], v[144:147], v[132:135], v[82:97]
	ds_read_b128 v[124:127], v103 offset:28672
	ds_read_b128 v[112:115], v101 offset:28672
	v_mfma_f32_32x32x16_f16 v[34:49], v[148:151], v[132:135], v[34:49]
	ds_read_b128 v[128:131], v103 offset:30720
	ds_read_b128 v[116:119], v101 offset:30720
	v_mfma_f32_32x32x16_f16 v[66:81], v[144:147], v[136:139], v[66:81]
	ds_read_b128 v[120:123], v101 offset:32768
	v_mfma_f32_32x32x16_f16 v[18:33], v[148:151], v[136:139], v[18:33]
	v_mfma_f32_32x32x16_f16 v[50:65], v[144:147], v[140:143], v[50:65]
	v_mfma_f32_32x32x16_f16 v[2:17], v[148:151], v[140:143], v[2:17]
	s_waitcnt lgkmcnt(0)
	v_mfma_f32_32x32x16_f16 v[82:97], v[124:127], v[112:115], v[82:97]
	ds_read_b128 v[144:147], v104 offset:28672
	ds_read_b128 v[132:135], v102 offset:28672
	v_mfma_f32_32x32x16_f16 v[34:49], v[128:131], v[112:115], v[34:49]
	ds_read_b128 v[148:151], v104 offset:30720
	ds_read_b128 v[136:139], v102 offset:30720
	v_mfma_f32_32x32x16_f16 v[66:81], v[124:127], v[116:119], v[66:81]
	ds_read_b128 v[140:143], v102 offset:32768
	v_mfma_f32_32x32x16_f16 v[18:33], v[128:131], v[116:119], v[18:33]
	v_mfma_f32_32x32x16_f16 v[50:65], v[124:127], v[120:123], v[50:65]
	v_mfma_f32_32x32x16_f16 v[2:17], v[128:131], v[120:123], v[2:17]
	s_waitcnt lgkmcnt(0)
	s_barrier
	v_mfma_f32_32x32x16_f16 v[82:97], v[144:147], v[132:135], v[82:97]
	ds_read_b128 v[124:127], v107
	ds_read_b128 v[112:115], v105
	v_mfma_f32_32x32x16_f16 v[34:49], v[148:151], v[132:135], v[34:49]
	ds_read_b128 v[128:131], v107 offset:2048
	ds_read_b128 v[116:119], v105 offset:2048
	v_mfma_f32_32x32x16_f16 v[66:81], v[144:147], v[136:139], v[66:81]
	ds_read_b128 v[120:123], v105 offset:4096
	v_mfma_f32_32x32x16_f16 v[18:33], v[148:151], v[136:139], v[18:33]
	v_mfma_f32_32x32x16_f16 v[50:65], v[144:147], v[140:143], v[50:65]
	v_mfma_f32_32x32x16_f16 v[2:17], v[148:151], v[140:143], v[2:17]
	s_waitcnt lgkmcnt(0)
	v_mfma_f32_32x32x16_f16 v[82:97], v[124:127], v[112:115], v[82:97]
	ds_read_b128 v[144:147], v108
	ds_read_b128 v[132:135], v106
	v_mfma_f32_32x32x16_f16 v[34:49], v[128:131], v[112:115], v[34:49]
	ds_read_b128 v[148:151], v108 offset:2048
	ds_read_b128 v[136:139], v106 offset:2048
	v_mfma_f32_32x32x16_f16 v[66:81], v[124:127], v[116:119], v[66:81]
	ds_read_b128 v[140:143], v106 offset:4096
	v_mfma_f32_32x32x16_f16 v[18:33], v[128:131], v[116:119], v[18:33]
	v_mfma_f32_32x32x16_f16 v[50:65], v[124:127], v[120:123], v[50:65]
	v_mfma_f32_32x32x16_f16 v[2:17], v[128:131], v[120:123], v[2:17]
	s_waitcnt lgkmcnt(0)
	s_barrier
	v_mfma_f32_32x32x16_f16 v[82:97], v[144:147], v[132:135], v[82:97]
	ds_read_b128 v[124:127], v107 offset:28672
	ds_read_b128 v[112:115], v105 offset:28672
	v_mfma_f32_32x32x16_f16 v[34:49], v[148:151], v[132:135], v[34:49]
	ds_read_b128 v[128:131], v107 offset:30720
	ds_read_b128 v[116:119], v105 offset:30720
	v_mfma_f32_32x32x16_f16 v[66:81], v[144:147], v[136:139], v[66:81]
	ds_read_b128 v[120:123], v105 offset:32768
	v_mfma_f32_32x32x16_f16 v[18:33], v[148:151], v[136:139], v[18:33]
	v_mfma_f32_32x32x16_f16 v[50:65], v[144:147], v[140:143], v[50:65]
	v_mfma_f32_32x32x16_f16 v[2:17], v[148:151], v[140:143], v[2:17]
	s_waitcnt lgkmcnt(0)
	v_mfma_f32_32x32x16_f16 v[82:97], v[124:127], v[112:115], v[82:97]
	ds_read_b128 v[144:147], v108 offset:28672
	ds_read_b128 v[132:135], v106 offset:28672
	v_mfma_f32_32x32x16_f16 v[34:49], v[128:131], v[112:115], v[34:49]
	ds_read_b128 v[148:151], v108 offset:30720
	ds_read_b128 v[136:139], v106 offset:30720
	v_mfma_f32_32x32x16_f16 v[66:81], v[124:127], v[116:119], v[66:81]
	ds_read_b128 v[140:143], v106 offset:32768
	v_mfma_f32_32x32x16_f16 v[18:33], v[128:131], v[116:119], v[18:33]
	v_mfma_f32_32x32x16_f16 v[50:65], v[124:127], v[120:123], v[50:65]
	v_mfma_f32_32x32x16_f16 v[2:17], v[128:131], v[120:123], v[2:17]
	s_waitcnt lgkmcnt(0)
	s_barrier
	v_mfma_f32_32x32x16_f16 v[82:97], v[144:147], v[132:135], v[82:97]
	ds_read_b128 v[124:127], v154
	ds_read_b128 v[112:115], v152
	v_mfma_f32_32x32x16_f16 v[34:49], v[148:151], v[132:135], v[34:49]
	ds_read_b128 v[128:131], v154 offset:2048
	ds_read_b128 v[116:119], v152 offset:2048
	v_mfma_f32_32x32x16_f16 v[66:81], v[144:147], v[136:139], v[66:81]
	ds_read_b128 v[120:123], v152 offset:4096
	v_mfma_f32_32x32x16_f16 v[18:33], v[148:151], v[136:139], v[18:33]
	v_mfma_f32_32x32x16_f16 v[50:65], v[144:147], v[140:143], v[50:65]
	v_mfma_f32_32x32x16_f16 v[2:17], v[148:151], v[140:143], v[2:17]
	s_waitcnt lgkmcnt(0)
	v_mfma_f32_32x32x16_f16 v[82:97], v[124:127], v[112:115], v[82:97]
	ds_read_b128 v[144:147], v155
	ds_read_b128 v[132:135], v153
	v_mfma_f32_32x32x16_f16 v[34:49], v[128:131], v[112:115], v[34:49]
	ds_read_b128 v[148:151], v155 offset:2048
	ds_read_b128 v[136:139], v153 offset:2048
	v_mfma_f32_32x32x16_f16 v[66:81], v[124:127], v[116:119], v[66:81]
	ds_read_b128 v[140:143], v153 offset:4096
	v_mfma_f32_32x32x16_f16 v[18:33], v[128:131], v[116:119], v[18:33]
	v_mfma_f32_32x32x16_f16 v[50:65], v[124:127], v[120:123], v[50:65]
	v_mfma_f32_32x32x16_f16 v[2:17], v[128:131], v[120:123], v[2:17]
	s_waitcnt lgkmcnt(0)
	s_barrier
	v_mfma_f32_32x32x16_f16 v[82:97], v[144:147], v[132:135], v[82:97]
	ds_read_b128 v[124:127], v103
	ds_read_b128 v[112:115], v101
	v_mfma_f32_32x32x16_f16 v[34:49], v[148:151], v[132:135], v[34:49]
	ds_read_b128 v[128:131], v103 offset:2048
	ds_read_b128 v[116:119], v101 offset:2048
	v_mfma_f32_32x32x16_f16 v[66:81], v[144:147], v[136:139], v[66:81]
	ds_read_b128 v[120:123], v101 offset:4096
	v_mfma_f32_32x32x16_f16 v[18:33], v[148:151], v[136:139], v[18:33]
	v_mfma_f32_32x32x16_f16 v[50:65], v[144:147], v[140:143], v[50:65]
	v_mfma_f32_32x32x16_f16 v[2:17], v[148:151], v[140:143], v[2:17]
	s_waitcnt lgkmcnt(0)
	v_mfma_f32_32x32x16_f16 v[82:97], v[124:127], v[112:115], v[82:97]
	ds_read_b128 v[144:147], v104
	ds_read_b128 v[132:135], v102
	v_mfma_f32_32x32x16_f16 v[34:49], v[128:131], v[112:115], v[34:49]
	ds_read_b128 v[148:151], v104 offset:2048
	ds_read_b128 v[136:139], v102 offset:2048
	v_mfma_f32_32x32x16_f16 v[66:81], v[124:127], v[116:119], v[66:81]
	ds_read_b128 v[140:143], v102 offset:4096
	v_mfma_f32_32x32x16_f16 v[18:33], v[128:131], v[116:119], v[18:33]
	v_mfma_f32_32x32x16_f16 v[50:65], v[124:127], v[120:123], v[50:65]
	v_mfma_f32_32x32x16_f16 v[2:17], v[128:131], v[120:123], v[2:17]
	s_waitcnt lgkmcnt(0)
	s_barrier
	v_mfma_f32_32x32x16_f16 v[82:97], v[144:147], v[132:135], v[82:97]
	ds_read_b128 v[124:127], v103 offset:28672
	ds_read_b128 v[112:115], v101 offset:28672
	v_mfma_f32_32x32x16_f16 v[34:49], v[148:151], v[132:135], v[34:49]
	ds_read_b128 v[128:131], v103 offset:30720
	ds_read_b128 v[116:119], v101 offset:30720
	v_mfma_f32_32x32x16_f16 v[66:81], v[144:147], v[136:139], v[66:81]
	ds_read_b128 v[120:123], v101 offset:32768
	v_mfma_f32_32x32x16_f16 v[18:33], v[148:151], v[136:139], v[18:33]
	v_mfma_f32_32x32x16_f16 v[50:65], v[144:147], v[140:143], v[50:65]
	v_mfma_f32_32x32x16_f16 v[2:17], v[148:151], v[140:143], v[2:17]
	s_waitcnt lgkmcnt(0)
	v_mfma_f32_32x32x16_f16 v[82:97], v[124:127], v[112:115], v[82:97]
	ds_read_b128 v[144:147], v104 offset:28672
	ds_read_b128 v[132:135], v102 offset:28672
	v_mfma_f32_32x32x16_f16 v[34:49], v[128:131], v[112:115], v[34:49]
	ds_read_b128 v[148:151], v104 offset:30720
	ds_read_b128 v[136:139], v102 offset:30720
	v_mfma_f32_32x32x16_f16 v[66:81], v[124:127], v[116:119], v[66:81]
	ds_read_b128 v[140:143], v102 offset:32768
	v_mfma_f32_32x32x16_f16 v[18:33], v[128:131], v[116:119], v[18:33]
	v_mfma_f32_32x32x16_f16 v[50:65], v[124:127], v[120:123], v[50:65]
	v_mfma_f32_32x32x16_f16 v[2:17], v[128:131], v[120:123], v[2:17]
	s_waitcnt lgkmcnt(0)
	s_barrier
	v_mfma_f32_32x32x16_f16 v[82:97], v[144:147], v[132:135], v[82:97]
	ds_read_b128 v[124:127], v107
	ds_read_b128 v[112:115], v105
	v_mfma_f32_32x32x16_f16 v[34:49], v[148:151], v[132:135], v[34:49]
	ds_read_b128 v[128:131], v107 offset:2048
	ds_read_b128 v[116:119], v105 offset:2048
	v_mfma_f32_32x32x16_f16 v[66:81], v[144:147], v[136:139], v[66:81]
	ds_read_b128 v[120:123], v105 offset:4096
	v_mfma_f32_32x32x16_f16 v[18:33], v[148:151], v[136:139], v[18:33]
	v_mfma_f32_32x32x16_f16 v[50:65], v[144:147], v[140:143], v[50:65]
	v_mfma_f32_32x32x16_f16 v[2:17], v[148:151], v[140:143], v[2:17]
	s_waitcnt lgkmcnt(0)
	v_mfma_f32_32x32x16_f16 v[82:97], v[124:127], v[112:115], v[82:97]
	ds_read_b128 v[144:147], v108
	ds_read_b128 v[132:135], v106
	v_mfma_f32_32x32x16_f16 v[34:49], v[128:131], v[112:115], v[34:49]
	ds_read_b128 v[148:151], v108 offset:2048
	ds_read_b128 v[136:139], v106 offset:2048
	v_mfma_f32_32x32x16_f16 v[66:81], v[124:127], v[116:119], v[66:81]
	ds_read_b128 v[140:143], v106 offset:4096
	v_mfma_f32_32x32x16_f16 v[18:33], v[128:131], v[116:119], v[18:33]
	v_mfma_f32_32x32x16_f16 v[50:65], v[124:127], v[120:123], v[50:65]
	v_mfma_f32_32x32x16_f16 v[2:17], v[128:131], v[120:123], v[2:17]
	s_waitcnt lgkmcnt(0)
	s_barrier
	v_mfma_f32_32x32x16_f16 v[82:97], v[144:147], v[132:135], v[82:97]
	ds_read_b128 v[124:127], v107 offset:28672
	ds_read_b128 v[112:115], v105 offset:28672
	v_mfma_f32_32x32x16_f16 v[34:49], v[148:151], v[132:135], v[34:49]
	ds_read_b128 v[128:131], v107 offset:30720
	ds_read_b128 v[116:119], v105 offset:30720
	v_mfma_f32_32x32x16_f16 v[66:81], v[144:147], v[136:139], v[66:81]
	ds_read_b128 v[120:123], v105 offset:32768
	v_mfma_f32_32x32x16_f16 v[18:33], v[148:151], v[136:139], v[18:33]
	v_mfma_f32_32x32x16_f16 v[50:65], v[144:147], v[140:143], v[50:65]
	v_mfma_f32_32x32x16_f16 v[2:17], v[148:151], v[140:143], v[2:17]
	s_waitcnt lgkmcnt(0)
	v_mfma_f32_32x32x16_f16 v[82:97], v[124:127], v[112:115], v[82:97]
	ds_read_b128 v[144:147], v108 offset:28672
	ds_read_b128 v[132:135], v106 offset:28672
	v_mfma_f32_32x32x16_f16 v[34:49], v[128:131], v[112:115], v[34:49]
	ds_read_b128 v[148:151], v108 offset:30720
	ds_read_b128 v[136:139], v106 offset:30720
	v_mfma_f32_32x32x16_f16 v[66:81], v[124:127], v[116:119], v[66:81]
	ds_read_b128 v[140:143], v106 offset:32768
	v_mfma_f32_32x32x16_f16 v[18:33], v[128:131], v[116:119], v[18:33]
	v_mfma_f32_32x32x16_f16 v[50:65], v[124:127], v[120:123], v[50:65]
	v_mfma_f32_32x32x16_f16 v[2:17], v[128:131], v[120:123], v[2:17]
	s_waitcnt lgkmcnt(0)
	s_barrier
	v_mfma_f32_32x32x16_f16 v[82:97], v[144:147], v[132:135], v[82:97]
	ds_read_b128 v[124:127], v154
	ds_read_b128 v[112:115], v152
	v_mfma_f32_32x32x16_f16 v[34:49], v[148:151], v[132:135], v[34:49]
	ds_read_b128 v[128:131], v154 offset:2048
	ds_read_b128 v[116:119], v152 offset:2048
	v_mfma_f32_32x32x16_f16 v[66:81], v[144:147], v[136:139], v[66:81]
	ds_read_b128 v[120:123], v152 offset:4096
	v_mfma_f32_32x32x16_f16 v[18:33], v[148:151], v[136:139], v[18:33]
	v_mfma_f32_32x32x16_f16 v[50:65], v[144:147], v[140:143], v[50:65]
	v_mfma_f32_32x32x16_f16 v[2:17], v[148:151], v[140:143], v[2:17]
	s_waitcnt lgkmcnt(0)
	v_mfma_f32_32x32x16_f16 v[82:97], v[124:127], v[112:115], v[82:97]
	ds_read_b128 v[144:147], v155
	ds_read_b128 v[132:135], v153
	v_mfma_f32_32x32x16_f16 v[34:49], v[128:131], v[112:115], v[34:49]
	ds_read_b128 v[148:151], v155 offset:2048
	ds_read_b128 v[136:139], v153 offset:2048
	v_mfma_f32_32x32x16_f16 v[66:81], v[124:127], v[116:119], v[66:81]
	ds_read_b128 v[140:143], v153 offset:4096
	v_mfma_f32_32x32x16_f16 v[18:33], v[128:131], v[116:119], v[18:33]
	v_mfma_f32_32x32x16_f16 v[50:65], v[124:127], v[120:123], v[50:65]
	v_mfma_f32_32x32x16_f16 v[2:17], v[128:131], v[120:123], v[2:17]
	s_waitcnt lgkmcnt(0)
	s_barrier
	v_mfma_f32_32x32x16_f16 v[82:97], v[144:147], v[132:135], v[82:97]
	ds_read_b128 v[124:127], v103
	ds_read_b128 v[112:115], v101
	v_mfma_f32_32x32x16_f16 v[34:49], v[148:151], v[132:135], v[34:49]
	ds_read_b128 v[128:131], v103 offset:2048
	ds_read_b128 v[116:119], v101 offset:2048
	v_mfma_f32_32x32x16_f16 v[66:81], v[144:147], v[136:139], v[66:81]
	ds_read_b128 v[120:123], v101 offset:4096
	v_mfma_f32_32x32x16_f16 v[18:33], v[148:151], v[136:139], v[18:33]
	v_mfma_f32_32x32x16_f16 v[50:65], v[144:147], v[140:143], v[50:65]
	v_mfma_f32_32x32x16_f16 v[2:17], v[148:151], v[140:143], v[2:17]
	s_waitcnt lgkmcnt(0)
	v_mfma_f32_32x32x16_f16 v[82:97], v[124:127], v[112:115], v[82:97]
	ds_read_b128 v[144:147], v104
	ds_read_b128 v[132:135], v102
	v_mfma_f32_32x32x16_f16 v[34:49], v[128:131], v[112:115], v[34:49]
	ds_read_b128 v[148:151], v104 offset:2048
	ds_read_b128 v[136:139], v102 offset:2048
	v_mfma_f32_32x32x16_f16 v[66:81], v[124:127], v[116:119], v[66:81]
	ds_read_b128 v[140:143], v102 offset:4096
	v_mfma_f32_32x32x16_f16 v[18:33], v[128:131], v[116:119], v[18:33]
	v_mfma_f32_32x32x16_f16 v[50:65], v[124:127], v[120:123], v[50:65]
	v_mfma_f32_32x32x16_f16 v[2:17], v[128:131], v[120:123], v[2:17]
	s_waitcnt lgkmcnt(0)
	s_barrier
	v_mfma_f32_32x32x16_f16 v[82:97], v[144:147], v[132:135], v[82:97]
	ds_read_b128 v[124:127], v103 offset:28672
	ds_read_b128 v[112:115], v101 offset:28672
	v_mfma_f32_32x32x16_f16 v[34:49], v[148:151], v[132:135], v[34:49]
	ds_read_b128 v[128:131], v103 offset:30720
	ds_read_b128 v[116:119], v101 offset:30720
	v_mfma_f32_32x32x16_f16 v[66:81], v[144:147], v[136:139], v[66:81]
	ds_read_b128 v[120:123], v101 offset:32768
	v_mfma_f32_32x32x16_f16 v[18:33], v[148:151], v[136:139], v[18:33]
	v_mfma_f32_32x32x16_f16 v[50:65], v[144:147], v[140:143], v[50:65]
	v_mfma_f32_32x32x16_f16 v[2:17], v[148:151], v[140:143], v[2:17]
	s_waitcnt lgkmcnt(0)
	v_mfma_f32_32x32x16_f16 v[82:97], v[124:127], v[112:115], v[82:97]
	ds_read_b128 v[144:147], v104 offset:28672
	ds_read_b128 v[132:135], v102 offset:28672
	v_mfma_f32_32x32x16_f16 v[34:49], v[128:131], v[112:115], v[34:49]
	ds_read_b128 v[148:151], v104 offset:30720
	ds_read_b128 v[136:139], v102 offset:30720
	v_mfma_f32_32x32x16_f16 v[66:81], v[124:127], v[116:119], v[66:81]
	ds_read_b128 v[140:143], v102 offset:32768
	v_mfma_f32_32x32x16_f16 v[18:33], v[128:131], v[116:119], v[18:33]
	v_mfma_f32_32x32x16_f16 v[50:65], v[124:127], v[120:123], v[50:65]
	v_mfma_f32_32x32x16_f16 v[2:17], v[128:131], v[120:123], v[2:17]
	s_waitcnt lgkmcnt(0)
	s_barrier
	v_mfma_f32_32x32x16_f16 v[82:97], v[144:147], v[132:135], v[82:97]
	ds_read_b128 v[124:127], v107
	ds_read_b128 v[112:115], v105
	v_mfma_f32_32x32x16_f16 v[34:49], v[148:151], v[132:135], v[34:49]
	ds_read_b128 v[128:131], v107 offset:2048
	ds_read_b128 v[116:119], v105 offset:2048
	v_mfma_f32_32x32x16_f16 v[66:81], v[144:147], v[136:139], v[66:81]
	ds_read_b128 v[120:123], v105 offset:4096
	v_mfma_f32_32x32x16_f16 v[18:33], v[148:151], v[136:139], v[18:33]
	v_mfma_f32_32x32x16_f16 v[50:65], v[144:147], v[140:143], v[50:65]
	v_mfma_f32_32x32x16_f16 v[2:17], v[148:151], v[140:143], v[2:17]
	s_waitcnt lgkmcnt(0)
	v_mfma_f32_32x32x16_f16 v[82:97], v[124:127], v[112:115], v[82:97]
	ds_read_b128 v[144:147], v108
	ds_read_b128 v[132:135], v106
	v_mfma_f32_32x32x16_f16 v[34:49], v[128:131], v[112:115], v[34:49]
	ds_read_b128 v[148:151], v108 offset:2048
	ds_read_b128 v[136:139], v106 offset:2048
	v_mfma_f32_32x32x16_f16 v[66:81], v[124:127], v[116:119], v[66:81]
	ds_read_b128 v[140:143], v106 offset:4096
	v_mfma_f32_32x32x16_f16 v[18:33], v[128:131], v[116:119], v[18:33]
	v_mfma_f32_32x32x16_f16 v[50:65], v[124:127], v[120:123], v[50:65]
	v_mfma_f32_32x32x16_f16 v[2:17], v[128:131], v[120:123], v[2:17]
	s_waitcnt lgkmcnt(0)
	s_barrier
	v_mfma_f32_32x32x16_f16 v[82:97], v[144:147], v[132:135], v[82:97]
	ds_read_b128 v[124:127], v107 offset:28672
	ds_read_b128 v[112:115], v105 offset:28672
	v_mfma_f32_32x32x16_f16 v[34:49], v[148:151], v[132:135], v[34:49]
	ds_read_b128 v[128:131], v107 offset:30720
	ds_read_b128 v[116:119], v105 offset:30720
	v_mfma_f32_32x32x16_f16 v[66:81], v[144:147], v[136:139], v[66:81]
	ds_read_b128 v[120:123], v105 offset:32768
	v_mfma_f32_32x32x16_f16 v[18:33], v[148:151], v[136:139], v[18:33]
	v_mfma_f32_32x32x16_f16 v[50:65], v[144:147], v[140:143], v[50:65]
	v_mfma_f32_32x32x16_f16 v[2:17], v[148:151], v[140:143], v[2:17]
	s_waitcnt lgkmcnt(0)
	v_mfma_f32_32x32x16_f16 v[82:97], v[124:127], v[112:115], v[82:97]
	ds_read_b128 v[144:147], v108 offset:28672
	ds_read_b128 v[132:135], v106 offset:28672
	v_mfma_f32_32x32x16_f16 v[34:49], v[128:131], v[112:115], v[34:49]
	ds_read_b128 v[148:151], v108 offset:30720
	ds_read_b128 v[136:139], v106 offset:30720
	v_mfma_f32_32x32x16_f16 v[66:81], v[124:127], v[116:119], v[66:81]
	ds_read_b128 v[140:143], v106 offset:32768
	v_mfma_f32_32x32x16_f16 v[18:33], v[128:131], v[116:119], v[18:33]
	v_mfma_f32_32x32x16_f16 v[50:65], v[124:127], v[120:123], v[50:65]
	v_mfma_f32_32x32x16_f16 v[2:17], v[128:131], v[120:123], v[2:17]
	s_waitcnt lgkmcnt(0)
	s_barrier
	v_mfma_f32_32x32x16_f16 v[82:97], v[144:147], v[132:135], v[82:97]
	ds_read_b128 v[124:127], v154
	ds_read_b128 v[112:115], v152
	v_mfma_f32_32x32x16_f16 v[34:49], v[148:151], v[132:135], v[34:49]
	ds_read_b128 v[128:131], v154 offset:2048
	ds_read_b128 v[116:119], v152 offset:2048
	v_mfma_f32_32x32x16_f16 v[66:81], v[144:147], v[136:139], v[66:81]
	ds_read_b128 v[120:123], v152 offset:4096
	v_mfma_f32_32x32x16_f16 v[18:33], v[148:151], v[136:139], v[18:33]
	v_mfma_f32_32x32x16_f16 v[50:65], v[144:147], v[140:143], v[50:65]
	v_mfma_f32_32x32x16_f16 v[2:17], v[148:151], v[140:143], v[2:17]
	s_waitcnt lgkmcnt(0)
	v_mfma_f32_32x32x16_f16 v[82:97], v[124:127], v[112:115], v[82:97]
	ds_read_b128 v[144:147], v155
	ds_read_b128 v[132:135], v153
	v_mfma_f32_32x32x16_f16 v[34:49], v[128:131], v[112:115], v[34:49]
	ds_read_b128 v[148:151], v155 offset:2048
	ds_read_b128 v[136:139], v153 offset:2048
	v_mfma_f32_32x32x16_f16 v[66:81], v[124:127], v[116:119], v[66:81]
	ds_read_b128 v[140:143], v153 offset:4096
	v_mfma_f32_32x32x16_f16 v[18:33], v[128:131], v[116:119], v[18:33]
	v_mfma_f32_32x32x16_f16 v[50:65], v[124:127], v[120:123], v[50:65]
	v_mfma_f32_32x32x16_f16 v[2:17], v[128:131], v[120:123], v[2:17]
	s_waitcnt lgkmcnt(0)
	s_barrier
	v_mfma_f32_32x32x16_f16 v[82:97], v[144:147], v[132:135], v[82:97]
	ds_read_b128 v[124:127], v103
	ds_read_b128 v[112:115], v101
	v_mfma_f32_32x32x16_f16 v[34:49], v[148:151], v[132:135], v[34:49]
	ds_read_b128 v[128:131], v103 offset:2048
	ds_read_b128 v[116:119], v101 offset:2048
	v_mfma_f32_32x32x16_f16 v[66:81], v[144:147], v[136:139], v[66:81]
	ds_read_b128 v[120:123], v101 offset:4096
	v_mfma_f32_32x32x16_f16 v[18:33], v[148:151], v[136:139], v[18:33]
	v_mfma_f32_32x32x16_f16 v[50:65], v[144:147], v[140:143], v[50:65]
	v_mfma_f32_32x32x16_f16 v[2:17], v[148:151], v[140:143], v[2:17]
	s_waitcnt lgkmcnt(0)
	v_mfma_f32_32x32x16_f16 v[82:97], v[124:127], v[112:115], v[82:97]
	ds_read_b128 v[144:147], v104
	ds_read_b128 v[132:135], v102
	v_mfma_f32_32x32x16_f16 v[34:49], v[128:131], v[112:115], v[34:49]
	ds_read_b128 v[148:151], v104 offset:2048
	ds_read_b128 v[136:139], v102 offset:2048
	v_mfma_f32_32x32x16_f16 v[66:81], v[124:127], v[116:119], v[66:81]
	ds_read_b128 v[140:143], v102 offset:4096
	v_mfma_f32_32x32x16_f16 v[18:33], v[128:131], v[116:119], v[18:33]
	v_mfma_f32_32x32x16_f16 v[50:65], v[124:127], v[120:123], v[50:65]
	v_mfma_f32_32x32x16_f16 v[2:17], v[128:131], v[120:123], v[2:17]
	s_waitcnt lgkmcnt(0)
	s_barrier
	v_mfma_f32_32x32x16_f16 v[82:97], v[144:147], v[132:135], v[82:97]
	ds_read_b128 v[124:127], v103 offset:28672
	ds_read_b128 v[112:115], v101 offset:28672
	v_mfma_f32_32x32x16_f16 v[34:49], v[148:151], v[132:135], v[34:49]
	ds_read_b128 v[128:131], v103 offset:30720
	ds_read_b128 v[116:119], v101 offset:30720
	v_mfma_f32_32x32x16_f16 v[66:81], v[144:147], v[136:139], v[66:81]
	ds_read_b128 v[120:123], v101 offset:32768
	v_mfma_f32_32x32x16_f16 v[18:33], v[148:151], v[136:139], v[18:33]
	v_mfma_f32_32x32x16_f16 v[50:65], v[144:147], v[140:143], v[50:65]
	v_mfma_f32_32x32x16_f16 v[2:17], v[148:151], v[140:143], v[2:17]
	s_waitcnt lgkmcnt(0)
	v_mfma_f32_32x32x16_f16 v[82:97], v[124:127], v[112:115], v[82:97]
	ds_read_b128 v[144:147], v104 offset:28672
	ds_read_b128 v[132:135], v102 offset:28672
	v_mfma_f32_32x32x16_f16 v[34:49], v[128:131], v[112:115], v[34:49]
	ds_read_b128 v[148:151], v104 offset:30720
	ds_read_b128 v[136:139], v102 offset:30720
	v_mfma_f32_32x32x16_f16 v[66:81], v[124:127], v[116:119], v[66:81]
	ds_read_b128 v[140:143], v102 offset:32768
	v_mfma_f32_32x32x16_f16 v[18:33], v[128:131], v[116:119], v[18:33]
	v_mfma_f32_32x32x16_f16 v[50:65], v[124:127], v[120:123], v[50:65]
	v_mfma_f32_32x32x16_f16 v[2:17], v[128:131], v[120:123], v[2:17]
	s_waitcnt lgkmcnt(0)
	s_barrier
	v_mfma_f32_32x32x16_f16 v[82:97], v[144:147], v[132:135], v[82:97]
	ds_read_b128 v[124:127], v107
	ds_read_b128 v[112:115], v105
	v_mfma_f32_32x32x16_f16 v[34:49], v[148:151], v[132:135], v[34:49]
	ds_read_b128 v[128:131], v107 offset:2048
	ds_read_b128 v[116:119], v105 offset:2048
	v_mfma_f32_32x32x16_f16 v[66:81], v[144:147], v[136:139], v[66:81]
	ds_read_b128 v[120:123], v105 offset:4096
	v_mfma_f32_32x32x16_f16 v[18:33], v[148:151], v[136:139], v[18:33]
	v_mfma_f32_32x32x16_f16 v[50:65], v[144:147], v[140:143], v[50:65]
	v_mfma_f32_32x32x16_f16 v[2:17], v[148:151], v[140:143], v[2:17]
	s_waitcnt lgkmcnt(0)
	v_mfma_f32_32x32x16_f16 v[82:97], v[124:127], v[112:115], v[82:97]
	ds_read_b128 v[144:147], v108
	ds_read_b128 v[132:135], v106
	v_mfma_f32_32x32x16_f16 v[34:49], v[128:131], v[112:115], v[34:49]
	ds_read_b128 v[148:151], v108 offset:2048
	ds_read_b128 v[136:139], v106 offset:2048
	v_mfma_f32_32x32x16_f16 v[66:81], v[124:127], v[116:119], v[66:81]
	ds_read_b128 v[140:143], v106 offset:4096
	v_mfma_f32_32x32x16_f16 v[18:33], v[128:131], v[116:119], v[18:33]
	v_mfma_f32_32x32x16_f16 v[50:65], v[124:127], v[120:123], v[50:65]
	v_mfma_f32_32x32x16_f16 v[2:17], v[128:131], v[120:123], v[2:17]
	s_waitcnt lgkmcnt(0)
	s_barrier
	v_mfma_f32_32x32x16_f16 v[82:97], v[144:147], v[132:135], v[82:97]
	ds_read_b128 v[124:127], v107 offset:28672
	ds_read_b128 v[112:115], v105 offset:28672
	v_mfma_f32_32x32x16_f16 v[34:49], v[148:151], v[132:135], v[34:49]
	ds_read_b128 v[128:131], v107 offset:30720
	ds_read_b128 v[116:119], v105 offset:30720
	v_mfma_f32_32x32x16_f16 v[66:81], v[144:147], v[136:139], v[66:81]
	ds_read_b128 v[120:123], v105 offset:32768
	v_mfma_f32_32x32x16_f16 v[18:33], v[148:151], v[136:139], v[18:33]
	v_mfma_f32_32x32x16_f16 v[50:65], v[144:147], v[140:143], v[50:65]
	v_mfma_f32_32x32x16_f16 v[2:17], v[148:151], v[140:143], v[2:17]
	s_waitcnt lgkmcnt(0)
	v_mfma_f32_32x32x16_f16 v[82:97], v[124:127], v[112:115], v[82:97]
	ds_read_b128 v[144:147], v108 offset:28672
	ds_read_b128 v[132:135], v106 offset:28672
	v_mfma_f32_32x32x16_f16 v[34:49], v[128:131], v[112:115], v[34:49]
	ds_read_b128 v[148:151], v108 offset:30720
	ds_read_b128 v[136:139], v106 offset:30720
	v_mfma_f32_32x32x16_f16 v[66:81], v[124:127], v[116:119], v[66:81]
	ds_read_b128 v[140:143], v106 offset:32768
	v_mfma_f32_32x32x16_f16 v[18:33], v[128:131], v[116:119], v[18:33]
	v_mfma_f32_32x32x16_f16 v[50:65], v[124:127], v[120:123], v[50:65]
	v_mfma_f32_32x32x16_f16 v[2:17], v[128:131], v[120:123], v[2:17]
	s_waitcnt lgkmcnt(0)
	v_mfma_f32_32x32x16_f16 v[82:97], v[144:147], v[132:135], v[82:97]
	v_mfma_f32_32x32x16_f16 v[34:49], v[148:151], v[132:135], v[34:49]
	v_mfma_f32_32x32x16_f16 v[66:81], v[144:147], v[136:139], v[66:81]
	v_mfma_f32_32x32x16_f16 v[18:33], v[148:151], v[136:139], v[18:33]
	v_mfma_f32_32x32x16_f16 v[50:65], v[144:147], v[140:143], v[50:65]
	v_mfma_f32_32x32x16_f16 v[2:17], v[148:151], v[140:143], v[2:17]

.LBB2_3:
	s_load_dwordx4 s[4:7], s[0:1], 0x10
	v_and_b32_e32 v51, 31, v1
	v_lshrrev_b32_e32 v50, 5, v1
	v_bfe_u32 v52, v1, 1, 3
	s_lshl_b32 s2, s13, 5
	v_or_b32_e32 v53, s2, v51
	v_lshlrev_b32_e32 v53, 7, v53
	v_add_u32_e32 v53, 0x800, v53
	v_lshlrev_b32_e32 v54, 7, v51
	v_add_u32_e32 v54, 0x4800, v54
	v_xor_b32_e32 v55, v50, v52
	v_lshlrev_b32_e32 v104, 4, v55
	v_add_u32_e32 v56, v53, v104
	v_add_u32_e32 v60, v54, v104
	v_add_u32_e32 v64, 0xe000, v56
	v_add_u32_e32 v68, 0xe000, v60
	v_add_u32_e32 v136, 0x1c000, v56
	v_add_u32_e32 v140, 0x1c000, v60
	v_xor_b32_e32 v104, 2, v55
	v_lshlrev_b32_e32 v104, 4, v104
	v_add_u32_e32 v57, v53, v104
	v_add_u32_e32 v61, v54, v104
	v_add_u32_e32 v65, 0xe000, v57
	v_add_u32_e32 v69, 0xe000, v61
	v_add_u32_e32 v137, 0x1c000, v57
	v_add_u32_e32 v141, 0x1c000, v61
	v_xor_b32_e32 v104, 4, v55
	v_lshlrev_b32_e32 v104, 4, v104
	v_add_u32_e32 v58, v53, v104
	v_add_u32_e32 v62, v54, v104
	v_add_u32_e32 v66, 0xe000, v58
	v_add_u32_e32 v70, 0xe000, v62
	v_add_u32_e32 v138, 0x1c000, v58
	v_add_u32_e32 v142, 0x1c000, v62
	v_xor_b32_e32 v104, 6, v55
	v_lshlrev_b32_e32 v104, 4, v104
	v_add_u32_e32 v59, v53, v104
	v_add_u32_e32 v63, v54, v104
	v_add_u32_e32 v67, 0xe000, v59
	v_add_u32_e32 v71, 0xe000, v63
	v_add_u32_e32 v139, 0x1c000, v59
	v_add_u32_e32 v143, 0x1c000, v63
	v_mov_b32_e32 v2, 0
	v_mov_b32_e32 v3, 0
	v_mov_b32_e32 v4, 0
	v_mov_b32_e32 v5, 0
	v_mov_b32_e32 v6, 0
	v_mov_b32_e32 v7, 0
	v_mov_b32_e32 v8, 0
	v_mov_b32_e32 v9, 0
	v_mov_b32_e32 v10, 0
	v_mov_b32_e32 v11, 0
	v_mov_b32_e32 v12, 0
	v_mov_b32_e32 v13, 0
	v_mov_b32_e32 v14, 0
	v_mov_b32_e32 v15, 0
	v_mov_b32_e32 v16, 0
	v_mov_b32_e32 v17, 0
	v_mov_b32_e32 v18, 0
	v_mov_b32_e32 v19, 0
	v_mov_b32_e32 v20, 0
	v_mov_b32_e32 v21, 0
	v_mov_b32_e32 v22, 0
	v_mov_b32_e32 v23, 0
	v_mov_b32_e32 v24, 0
	v_mov_b32_e32 v25, 0
	v_mov_b32_e32 v26, 0
	v_mov_b32_e32 v27, 0
	v_mov_b32_e32 v28, 0
	v_mov_b32_e32 v29, 0
	v_mov_b32_e32 v30, 0
	v_mov_b32_e32 v31, 0
	v_mov_b32_e32 v32, 0
	v_mov_b32_e32 v33, 0
	v_mov_b32_e32 v34, 0
	v_mov_b32_e32 v35, 0
	v_mov_b32_e32 v36, 0
	v_mov_b32_e32 v37, 0
	v_mov_b32_e32 v38, 0
	v_mov_b32_e32 v39, 0
	v_mov_b32_e32 v40, 0
	v_mov_b32_e32 v41, 0
	v_mov_b32_e32 v42, 0
	v_mov_b32_e32 v43, 0
	v_mov_b32_e32 v44, 0
	v_mov_b32_e32 v45, 0
	v_mov_b32_e32 v46, 0
	v_mov_b32_e32 v47, 0
	v_mov_b32_e32 v48, 0
	v_mov_b32_e32 v49, 0
	s_barrier
	ds_read_b128 v[72:75], v56
	ds_read_b128 v[76:79], v60
	ds_read_b128 v[80:83], v60 offset:4096
	ds_read_b128 v[84:87], v60 offset:8192
	ds_read_b128 v[88:91], v57
	ds_read_b128 v[92:95], v61
	ds_read_b128 v[96:99], v61 offset:4096
	ds_read_b128 v[100:103], v61 offset:8192
	s_waitcnt lgkmcnt(0)
	v_mfma_f32_32x32x16_f16 v[34:49], v[72:75], v[76:79], v[34:49]
	ds_read_b128 v[104:107], v58
	ds_read_b128 v[108:111], v62
	v_mfma_f32_32x32x16_f16 v[18:33], v[72:75], v[80:83], v[18:33]
	ds_read_b128 v[112:115], v62 offset:4096
	ds_read_b128 v[116:119], v62 offset:8192
	v_mfma_f32_32x32x16_f16 v[2:17], v[72:75], v[84:87], v[2:17]
	ds_read_b128 v[120:123], v59
	ds_read_b128 v[124:127], v63
	v_mfma_f32_32x32x16_f16 v[34:49], v[88:91], v[92:95], v[34:49]
	ds_read_b128 v[128:131], v63 offset:4096
	ds_read_b128 v[132:135], v63 offset:8192
	v_mfma_f32_32x32x16_f16 v[18:33], v[88:91], v[96:99], v[18:33]
	v_mfma_f32_32x32x16_f16 v[2:17], v[88:91], v[100:103], v[2:17]
	s_waitcnt lgkmcnt(0)
	s_barrier
	v_mfma_f32_32x32x16_f16 v[34:49], v[104:107], v[108:111], v[34:49]
	ds_read_b128 v[72:75], v56 offset:28672
	ds_read_b128 v[76:79], v60 offset:28672
	v_mfma_f32_32x32x16_f16 v[18:33], v[104:107], v[112:115], v[18:33]
	ds_read_b128 v[80:83], v60 offset:32768
	ds_read_b128 v[84:87], v60 offset:36864
	v_mfma_f32_32x32x16_f16 v[2:17], v[104:107], v[116:119], v[2:17]
	ds_read_b128 v[88:91], v57 offset:28672
	ds_read_b128 v[92:95], v61 offset:28672
	v_mfma_f32_32x32x16_f16 v[34:49], v[120:123], v[124:127], v[34:49]
	ds_read_b128 v[96:99], v61 offset:32768
	ds_read_b128 v[100:103], v61 offset:36864
	v_mfma_f32_32x32x16_f16 v[18:33], v[120:123], v[128:131], v[18:33]
	v_mfma_f32_32x32x16_f16 v[2:17], v[120:123], v[132:135], v[2:17]
	s_waitcnt lgkmcnt(0)
	v_mfma_f32_32x32x16_f16 v[34:49], v[72:75], v[76:79], v[34:49]
	ds_read_b128 v[104:107], v58 offset:28672
	ds_read_b128 v[108:111], v62 offset:28672
	v_mfma_f32_32x32x16_f16 v[18:33], v[72:75], v[80:83], v[18:33]
	ds_read_b128 v[112:115], v62 offset:32768
	ds_read_b128 v[116:119], v62 offset:36864
	v_mfma_f32_32x32x16_f16 v[2:17], v[72:75], v[84:87], v[2:17]
	ds_read_b128 v[120:123], v59 offset:28672
	ds_read_b128 v[124:127], v63 offset:28672
	v_mfma_f32_32x32x16_f16 v[34:49], v[88:91], v[92:95], v[34:49]
	ds_read_b128 v[128:131], v63 offset:32768
	ds_read_b128 v[132:135], v63 offset:36864
	v_mfma_f32_32x32x16_f16 v[18:33], v[88:91], v[96:99], v[18:33]
	v_mfma_f32_32x32x16_f16 v[2:17], v[88:91], v[100:103], v[2:17]
	s_waitcnt lgkmcnt(0)
	s_barrier
	v_mfma_f32_32x32x16_f16 v[34:49], v[104:107], v[108:111], v[34:49]
	ds_read_b128 v[72:75], v64
	ds_read_b128 v[76:79], v68
	v_mfma_f32_32x32x16_f16 v[18:33], v[104:107], v[112:115], v[18:33]
	ds_read_b128 v[80:83], v68 offset:4096
	ds_read_b128 v[84:87], v68 offset:8192
	v_mfma_f32_32x32x16_f16 v[2:17], v[104:107], v[116:119], v[2:17]
	ds_read_b128 v[88:91], v65
	ds_read_b128 v[92:95], v69
	v_mfma_f32_32x32x16_f16 v[34:49], v[120:123], v[124:127], v[34:49]
	ds_read_b128 v[96:99], v69 offset:4096
	ds_read_b128 v[100:103], v69 offset:8192
	v_mfma_f32_32x32x16_f16 v[18:33], v[120:123], v[128:131], v[18:33]
	v_mfma_f32_32x32x16_f16 v[2:17], v[120:123], v[132:135], v[2:17]
	s_waitcnt lgkmcnt(0)
	v_mfma_f32_32x32x16_f16 v[34:49], v[72:75], v[76:79], v[34:49]
	ds_read_b128 v[104:107], v66
	ds_read_b128 v[108:111], v70
	v_mfma_f32_32x32x16_f16 v[18:33], v[72:75], v[80:83], v[18:33]
	ds_read_b128 v[112:115], v70 offset:4096
	ds_read_b128 v[116:119], v70 offset:8192
	v_mfma_f32_32x32x16_f16 v[2:17], v[72:75], v[84:87], v[2:17]
	ds_read_b128 v[120:123], v67
	ds_read_b128 v[124:127], v71
	v_mfma_f32_32x32x16_f16 v[34:49], v[88:91], v[92:95], v[34:49]
	ds_read_b128 v[128:131], v71 offset:4096
	ds_read_b128 v[132:135], v71 offset:8192
	v_mfma_f32_32x32x16_f16 v[18:33], v[88:91], v[96:99], v[18:33]
	v_mfma_f32_32x32x16_f16 v[2:17], v[88:91], v[100:103], v[2:17]
	s_waitcnt lgkmcnt(0)
	s_barrier
	v_mfma_f32_32x32x16_f16 v[34:49], v[104:107], v[108:111], v[34:49]
	ds_read_b128 v[72:75], v64 offset:28672
	ds_read_b128 v[76:79], v68 offset:28672
	v_mfma_f32_32x32x16_f16 v[18:33], v[104:107], v[112:115], v[18:33]
	ds_read_b128 v[80:83], v68 offset:32768
	ds_read_b128 v[84:87], v68 offset:36864
	v_mfma_f32_32x32x16_f16 v[2:17], v[104:107], v[116:119], v[2:17]
	ds_read_b128 v[88:91], v65 offset:28672
	ds_read_b128 v[92:95], v69 offset:28672
	v_mfma_f32_32x32x16_f16 v[34:49], v[120:123], v[124:127], v[34:49]
	ds_read_b128 v[96:99], v69 offset:32768
	ds_read_b128 v[100:103], v69 offset:36864
	v_mfma_f32_32x32x16_f16 v[18:33], v[120:123], v[128:131], v[18:33]
	v_mfma_f32_32x32x16_f16 v[2:17], v[120:123], v[132:135], v[2:17]
	s_waitcnt lgkmcnt(0)
	v_mfma_f32_32x32x16_f16 v[34:49], v[72:75], v[76:79], v[34:49]
	ds_read_b128 v[104:107], v66 offset:28672
	ds_read_b128 v[108:111], v70 offset:28672
	v_mfma_f32_32x32x16_f16 v[18:33], v[72:75], v[80:83], v[18:33]
	ds_read_b128 v[112:115], v70 offset:32768
	ds_read_b128 v[116:119], v70 offset:36864
	v_mfma_f32_32x32x16_f16 v[2:17], v[72:75], v[84:87], v[2:17]
	ds_read_b128 v[120:123], v67 offset:28672
	ds_read_b128 v[124:127], v71 offset:28672
	v_mfma_f32_32x32x16_f16 v[34:49], v[88:91], v[92:95], v[34:49]
	ds_read_b128 v[128:131], v71 offset:32768
	ds_read_b128 v[132:135], v71 offset:36864
	v_mfma_f32_32x32x16_f16 v[18:33], v[88:91], v[96:99], v[18:33]
	v_mfma_f32_32x32x16_f16 v[2:17], v[88:91], v[100:103], v[2:17]
	s_waitcnt lgkmcnt(0)
	s_barrier
	v_mfma_f32_32x32x16_f16 v[34:49], v[104:107], v[108:111], v[34:49]
	ds_read_b128 v[72:75], v136
	ds_read_b128 v[76:79], v140
	v_mfma_f32_32x32x16_f16 v[18:33], v[104:107], v[112:115], v[18:33]
	ds_read_b128 v[80:83], v140 offset:4096
	ds_read_b128 v[84:87], v140 offset:8192
	v_mfma_f32_32x32x16_f16 v[2:17], v[104:107], v[116:119], v[2:17]
	ds_read_b128 v[88:91], v137
	ds_read_b128 v[92:95], v141
	v_mfma_f32_32x32x16_f16 v[34:49], v[120:123], v[124:127], v[34:49]
	ds_read_b128 v[96:99], v141 offset:4096
	ds_read_b128 v[100:103], v141 offset:8192
	v_mfma_f32_32x32x16_f16 v[18:33], v[120:123], v[128:131], v[18:33]
	v_mfma_f32_32x32x16_f16 v[2:17], v[120:123], v[132:135], v[2:17]
	s_waitcnt lgkmcnt(0)
	v_mfma_f32_32x32x16_f16 v[34:49], v[72:75], v[76:79], v[34:49]
	ds_read_b128 v[104:107], v138
	ds_read_b128 v[108:111], v142
	v_mfma_f32_32x32x16_f16 v[18:33], v[72:75], v[80:83], v[18:33]
	ds_read_b128 v[112:115], v142 offset:4096
	ds_read_b128 v[116:119], v142 offset:8192
	v_mfma_f32_32x32x16_f16 v[2:17], v[72:75], v[84:87], v[2:17]
	ds_read_b128 v[120:123], v139
	ds_read_b128 v[124:127], v143
	v_mfma_f32_32x32x16_f16 v[34:49], v[88:91], v[92:95], v[34:49]
	ds_read_b128 v[128:131], v143 offset:4096
	ds_read_b128 v[132:135], v143 offset:8192
	v_mfma_f32_32x32x16_f16 v[18:33], v[88:91], v[96:99], v[18:33]
	v_mfma_f32_32x32x16_f16 v[2:17], v[88:91], v[100:103], v[2:17]
	s_waitcnt lgkmcnt(0)
	s_barrier
	v_mfma_f32_32x32x16_f16 v[34:49], v[104:107], v[108:111], v[34:49]
	ds_read_b128 v[72:75], v56
	ds_read_b128 v[76:79], v60
	v_mfma_f32_32x32x16_f16 v[18:33], v[104:107], v[112:115], v[18:33]
	ds_read_b128 v[80:83], v60 offset:4096
	ds_read_b128 v[84:87], v60 offset:8192
	v_mfma_f32_32x32x16_f16 v[2:17], v[104:107], v[116:119], v[2:17]
	ds_read_b128 v[88:91], v57
	ds_read_b128 v[92:95], v61
	v_mfma_f32_32x32x16_f16 v[34:49], v[120:123], v[124:127], v[34:49]
	ds_read_b128 v[96:99], v61 offset:4096
	ds_read_b128 v[100:103], v61 offset:8192
	v_mfma_f32_32x32x16_f16 v[18:33], v[120:123], v[128:131], v[18:33]
	v_mfma_f32_32x32x16_f16 v[2:17], v[120:123], v[132:135], v[2:17]
	s_waitcnt lgkmcnt(0)
	v_mfma_f32_32x32x16_f16 v[34:49], v[72:75], v[76:79], v[34:49]
	ds_read_b128 v[104:107], v58
	ds_read_b128 v[108:111], v62
	v_mfma_f32_32x32x16_f16 v[18:33], v[72:75], v[80:83], v[18:33]
	ds_read_b128 v[112:115], v62 offset:4096
	ds_read_b128 v[116:119], v62 offset:8192
	v_mfma_f32_32x32x16_f16 v[2:17], v[72:75], v[84:87], v[2:17]
	ds_read_b128 v[120:123], v59
	ds_read_b128 v[124:127], v63
	v_mfma_f32_32x32x16_f16 v[34:49], v[88:91], v[92:95], v[34:49]
	ds_read_b128 v[128:131], v63 offset:4096
	ds_read_b128 v[132:135], v63 offset:8192
	v_mfma_f32_32x32x16_f16 v[18:33], v[88:91], v[96:99], v[18:33]
	v_mfma_f32_32x32x16_f16 v[2:17], v[88:91], v[100:103], v[2:17]
	s_waitcnt lgkmcnt(0)
	s_barrier
	v_mfma_f32_32x32x16_f16 v[34:49], v[104:107], v[108:111], v[34:49]
	ds_read_b128 v[72:75], v56 offset:28672
	ds_read_b128 v[76:79], v60 offset:28672
	v_mfma_f32_32x32x16_f16 v[18:33], v[104:107], v[112:115], v[18:33]
	ds_read_b128 v[80:83], v60 offset:32768
	ds_read_b128 v[84:87], v60 offset:36864
	v_mfma_f32_32x32x16_f16 v[2:17], v[104:107], v[116:119], v[2:17]
	ds_read_b128 v[88:91], v57 offset:28672
	ds_read_b128 v[92:95], v61 offset:28672
	v_mfma_f32_32x32x16_f16 v[34:49], v[120:123], v[124:127], v[34:49]
	ds_read_b128 v[96:99], v61 offset:32768
	ds_read_b128 v[100:103], v61 offset:36864
	v_mfma_f32_32x32x16_f16 v[18:33], v[120:123], v[128:131], v[18:33]
	v_mfma_f32_32x32x16_f16 v[2:17], v[120:123], v[132:135], v[2:17]
	s_waitcnt lgkmcnt(0)
	v_mfma_f32_32x32x16_f16 v[34:49], v[72:75], v[76:79], v[34:49]
	ds_read_b128 v[104:107], v58 offset:28672
	ds_read_b128 v[108:111], v62 offset:28672
	v_mfma_f32_32x32x16_f16 v[18:33], v[72:75], v[80:83], v[18:33]
	ds_read_b128 v[112:115], v62 offset:32768
	ds_read_b128 v[116:119], v62 offset:36864
	v_mfma_f32_32x32x16_f16 v[2:17], v[72:75], v[84:87], v[2:17]
	ds_read_b128 v[120:123], v59 offset:28672
	ds_read_b128 v[124:127], v63 offset:28672
	v_mfma_f32_32x32x16_f16 v[34:49], v[88:91], v[92:95], v[34:49]
	ds_read_b128 v[128:131], v63 offset:32768
	ds_read_b128 v[132:135], v63 offset:36864
	v_mfma_f32_32x32x16_f16 v[18:33], v[88:91], v[96:99], v[18:33]
	v_mfma_f32_32x32x16_f16 v[2:17], v[88:91], v[100:103], v[2:17]
	s_waitcnt lgkmcnt(0)
	s_barrier
	v_mfma_f32_32x32x16_f16 v[34:49], v[104:107], v[108:111], v[34:49]
	ds_read_b128 v[72:75], v64
	ds_read_b128 v[76:79], v68
	v_mfma_f32_32x32x16_f16 v[18:33], v[104:107], v[112:115], v[18:33]
	ds_read_b128 v[80:83], v68 offset:4096
	ds_read_b128 v[84:87], v68 offset:8192
	v_mfma_f32_32x32x16_f16 v[2:17], v[104:107], v[116:119], v[2:17]
	ds_read_b128 v[88:91], v65
	ds_read_b128 v[92:95], v69
	v_mfma_f32_32x32x16_f16 v[34:49], v[120:123], v[124:127], v[34:49]
	ds_read_b128 v[96:99], v69 offset:4096
	ds_read_b128 v[100:103], v69 offset:8192
	v_mfma_f32_32x32x16_f16 v[18:33], v[120:123], v[128:131], v[18:33]
	v_mfma_f32_32x32x16_f16 v[2:17], v[120:123], v[132:135], v[2:17]
	s_waitcnt lgkmcnt(0)
	v_mfma_f32_32x32x16_f16 v[34:49], v[72:75], v[76:79], v[34:49]
	ds_read_b128 v[104:107], v66
	ds_read_b128 v[108:111], v70
	v_mfma_f32_32x32x16_f16 v[18:33], v[72:75], v[80:83], v[18:33]
	ds_read_b128 v[112:115], v70 offset:4096
	ds_read_b128 v[116:119], v70 offset:8192
	v_mfma_f32_32x32x16_f16 v[2:17], v[72:75], v[84:87], v[2:17]
	ds_read_b128 v[120:123], v67
	ds_read_b128 v[124:127], v71
	v_mfma_f32_32x32x16_f16 v[34:49], v[88:91], v[92:95], v[34:49]
	ds_read_b128 v[128:131], v71 offset:4096
	ds_read_b128 v[132:135], v71 offset:8192
	v_mfma_f32_32x32x16_f16 v[18:33], v[88:91], v[96:99], v[18:33]
	v_mfma_f32_32x32x16_f16 v[2:17], v[88:91], v[100:103], v[2:17]
	s_waitcnt lgkmcnt(0)
	s_barrier
	v_mfma_f32_32x32x16_f16 v[34:49], v[104:107], v[108:111], v[34:49]
	ds_read_b128 v[72:75], v64 offset:28672
	ds_read_b128 v[76:79], v68 offset:28672
	v_mfma_f32_32x32x16_f16 v[18:33], v[104:107], v[112:115], v[18:33]
	ds_read_b128 v[80:83], v68 offset:32768
	ds_read_b128 v[84:87], v68 offset:36864
	v_mfma_f32_32x32x16_f16 v[2:17], v[104:107], v[116:119], v[2:17]
	ds_read_b128 v[88:91], v65 offset:28672
	ds_read_b128 v[92:95], v69 offset:28672
	v_mfma_f32_32x32x16_f16 v[34:49], v[120:123], v[124:127], v[34:49]
	ds_read_b128 v[96:99], v69 offset:32768
	ds_read_b128 v[100:103], v69 offset:36864
	v_mfma_f32_32x32x16_f16 v[18:33], v[120:123], v[128:131], v[18:33]
	v_mfma_f32_32x32x16_f16 v[2:17], v[120:123], v[132:135], v[2:17]
	s_waitcnt lgkmcnt(0)
	v_mfma_f32_32x32x16_f16 v[34:49], v[72:75], v[76:79], v[34:49]
	ds_read_b128 v[104:107], v66 offset:28672
	ds_read_b128 v[108:111], v70 offset:28672
	v_mfma_f32_32x32x16_f16 v[18:33], v[72:75], v[80:83], v[18:33]
	ds_read_b128 v[112:115], v70 offset:32768
	ds_read_b128 v[116:119], v70 offset:36864
	v_mfma_f32_32x32x16_f16 v[2:17], v[72:75], v[84:87], v[2:17]
	ds_read_b128 v[120:123], v67 offset:28672
	ds_read_b128 v[124:127], v71 offset:28672
	v_mfma_f32_32x32x16_f16 v[34:49], v[88:91], v[92:95], v[34:49]
	ds_read_b128 v[128:131], v71 offset:32768
	ds_read_b128 v[132:135], v71 offset:36864
	v_mfma_f32_32x32x16_f16 v[18:33], v[88:91], v[96:99], v[18:33]
	v_mfma_f32_32x32x16_f16 v[2:17], v[88:91], v[100:103], v[2:17]
	s_waitcnt lgkmcnt(0)
	s_barrier
	v_mfma_f32_32x32x16_f16 v[34:49], v[104:107], v[108:111], v[34:49]
	ds_read_b128 v[72:75], v136
	ds_read_b128 v[76:79], v140
	v_mfma_f32_32x32x16_f16 v[18:33], v[104:107], v[112:115], v[18:33]
	ds_read_b128 v[80:83], v140 offset:4096
	ds_read_b128 v[84:87], v140 offset:8192
	v_mfma_f32_32x32x16_f16 v[2:17], v[104:107], v[116:119], v[2:17]
	ds_read_b128 v[88:91], v137
	ds_read_b128 v[92:95], v141
	v_mfma_f32_32x32x16_f16 v[34:49], v[120:123], v[124:127], v[34:49]
	ds_read_b128 v[96:99], v141 offset:4096
	ds_read_b128 v[100:103], v141 offset:8192
	v_mfma_f32_32x32x16_f16 v[18:33], v[120:123], v[128:131], v[18:33]
	v_mfma_f32_32x32x16_f16 v[2:17], v[120:123], v[132:135], v[2:17]
	s_waitcnt lgkmcnt(0)
	v_mfma_f32_32x32x16_f16 v[34:49], v[72:75], v[76:79], v[34:49]
	ds_read_b128 v[104:107], v138
	ds_read_b128 v[108:111], v142
	v_mfma_f32_32x32x16_f16 v[18:33], v[72:75], v[80:83], v[18:33]
	ds_read_b128 v[112:115], v142 offset:4096
	ds_read_b128 v[116:119], v142 offset:8192
	v_mfma_f32_32x32x16_f16 v[2:17], v[72:75], v[84:87], v[2:17]
	ds_read_b128 v[120:123], v139
	ds_read_b128 v[124:127], v143
	v_mfma_f32_32x32x16_f16 v[34:49], v[88:91], v[92:95], v[34:49]
	ds_read_b128 v[128:131], v143 offset:4096
	ds_read_b128 v[132:135], v143 offset:8192
	v_mfma_f32_32x32x16_f16 v[18:33], v[88:91], v[96:99], v[18:33]
	v_mfma_f32_32x32x16_f16 v[2:17], v[88:91], v[100:103], v[2:17]
	s_waitcnt lgkmcnt(0)
	s_barrier
	v_mfma_f32_32x32x16_f16 v[34:49], v[104:107], v[108:111], v[34:49]
	ds_read_b128 v[72:75], v56
	ds_read_b128 v[76:79], v60
	v_mfma_f32_32x32x16_f16 v[18:33], v[104:107], v[112:115], v[18:33]
	ds_read_b128 v[80:83], v60 offset:4096
	ds_read_b128 v[84:87], v60 offset:8192
	v_mfma_f32_32x32x16_f16 v[2:17], v[104:107], v[116:119], v[2:17]
	ds_read_b128 v[88:91], v57
	ds_read_b128 v[92:95], v61
	v_mfma_f32_32x32x16_f16 v[34:49], v[120:123], v[124:127], v[34:49]
	ds_read_b128 v[96:99], v61 offset:4096
	ds_read_b128 v[100:103], v61 offset:8192
	v_mfma_f32_32x32x16_f16 v[18:33], v[120:123], v[128:131], v[18:33]
	v_mfma_f32_32x32x16_f16 v[2:17], v[120:123], v[132:135], v[2:17]
	s_waitcnt lgkmcnt(0)
	v_mfma_f32_32x32x16_f16 v[34:49], v[72:75], v[76:79], v[34:49]
	ds_read_b128 v[104:107], v58
	ds_read_b128 v[108:111], v62
	v_mfma_f32_32x32x16_f16 v[18:33], v[72:75], v[80:83], v[18:33]
	ds_read_b128 v[112:115], v62 offset:4096
	ds_read_b128 v[116:119], v62 offset:8192
	v_mfma_f32_32x32x16_f16 v[2:17], v[72:75], v[84:87], v[2:17]
	ds_read_b128 v[120:123], v59
	ds_read_b128 v[124:127], v63
	v_mfma_f32_32x32x16_f16 v[34:49], v[88:91], v[92:95], v[34:49]
	ds_read_b128 v[128:131], v63 offset:4096
	ds_read_b128 v[132:135], v63 offset:8192
	v_mfma_f32_32x32x16_f16 v[18:33], v[88:91], v[96:99], v[18:33]
	v_mfma_f32_32x32x16_f16 v[2:17], v[88:91], v[100:103], v[2:17]
	s_waitcnt lgkmcnt(0)
	s_barrier
	v_mfma_f32_32x32x16_f16 v[34:49], v[104:107], v[108:111], v[34:49]
	ds_read_b128 v[72:75], v56 offset:28672
	ds_read_b128 v[76:79], v60 offset:28672
	v_mfma_f32_32x32x16_f16 v[18:33], v[104:107], v[112:115], v[18:33]
	ds_read_b128 v[80:83], v60 offset:32768
	ds_read_b128 v[84:87], v60 offset:36864
	v_mfma_f32_32x32x16_f16 v[2:17], v[104:107], v[116:119], v[2:17]
	ds_read_b128 v[88:91], v57 offset:28672
	ds_read_b128 v[92:95], v61 offset:28672
	v_mfma_f32_32x32x16_f16 v[34:49], v[120:123], v[124:127], v[34:49]
	ds_read_b128 v[96:99], v61 offset:32768
	ds_read_b128 v[100:103], v61 offset:36864
	v_mfma_f32_32x32x16_f16 v[18:33], v[120:123], v[128:131], v[18:33]
	v_mfma_f32_32x32x16_f16 v[2:17], v[120:123], v[132:135], v[2:17]
	s_waitcnt lgkmcnt(0)
	v_mfma_f32_32x32x16_f16 v[34:49], v[72:75], v[76:79], v[34:49]
	ds_read_b128 v[104:107], v58 offset:28672
	ds_read_b128 v[108:111], v62 offset:28672
	v_mfma_f32_32x32x16_f16 v[18:33], v[72:75], v[80:83], v[18:33]
	ds_read_b128 v[112:115], v62 offset:32768
	ds_read_b128 v[116:119], v62 offset:36864
	v_mfma_f32_32x32x16_f16 v[2:17], v[72:75], v[84:87], v[2:17]
	ds_read_b128 v[120:123], v59 offset:28672
	ds_read_b128 v[124:127], v63 offset:28672
	v_mfma_f32_32x32x16_f16 v[34:49], v[88:91], v[92:95], v[34:49]
	ds_read_b128 v[128:131], v63 offset:32768
	ds_read_b128 v[132:135], v63 offset:36864
	v_mfma_f32_32x32x16_f16 v[18:33], v[88:91], v[96:99], v[18:33]
	v_mfma_f32_32x32x16_f16 v[2:17], v[88:91], v[100:103], v[2:17]
	s_waitcnt lgkmcnt(0)
	v_mfma_f32_32x32x16_f16 v[34:49], v[104:107], v[108:111], v[34:49]
	v_mfma_f32_32x32x16_f16 v[18:33], v[104:107], v[112:115], v[18:33]
	v_mfma_f32_32x32x16_f16 v[2:17], v[104:107], v[116:119], v[2:17]
	v_mfma_f32_32x32x16_f16 v[34:49], v[120:123], v[124:127], v[34:49]
	v_mfma_f32_32x32x16_f16 v[18:33], v[120:123], v[128:131], v[18:33]
	v_mfma_f32_32x32x16_f16 v[2:17], v[120:123], v[132:135], v[2:17]
	v_add_u32_e32 v51, s9, v51
	v_lshlrev_b32_e32 v104, 2, v51
	global_load_dword v105, v104, s[4:5]
	global_load_dword v106, v104, s[4:5] offset:128
	global_load_dword v107, v104, s[4:5] offset:256
	s_add_i32 s2, s2, s8
	v_lshl_add_u32 v108, v50, 2, s2
	v_mul_u32_u24_e32 v108, 0xc00, v108
	v_add_u32_e32 v108, v108, v104
	s_waitcnt vmcnt(0)
	s_nop 15
	v_add_f32_e32 v110, v105, v34
	v_add_f32_e32 v111, v106, v18
	v_add_f32_e32 v112, v107, v2
	global_store_dword v108, v110, s[6:7] nt
	global_store_dword v108, v111, s[6:7] offset:128 nt
	global_store_dword v108, v112, s[6:7] offset:256 nt
	v_add_u32_e32 v109, 0xc00, v108
	v_add_f32_e32 v110, v105, v35
	v_add_f32_e32 v111, v106, v19
	v_add_f32_e32 v112, v107, v3
	global_store_dword v109, v110, s[6:7] nt
	global_store_dword v109, v111, s[6:7] offset:128 nt
	global_store_dword v109, v112, s[6:7] offset:256 nt
	v_add_u32_e32 v109, 0x1800, v108
	v_add_f32_e32 v110, v105, v36
	v_add_f32_e32 v111, v106, v20
	v_add_f32_e32 v112, v107, v4
	global_store_dword v109, v110, s[6:7] nt
	global_store_dword v109, v111, s[6:7] offset:128 nt
	global_store_dword v109, v112, s[6:7] offset:256 nt
	v_add_u32_e32 v109, 0x2400, v108
	v_add_f32_e32 v110, v105, v37
	v_add_f32_e32 v111, v106, v21
	v_add_f32_e32 v112, v107, v5
	global_store_dword v109, v110, s[6:7] nt
	global_store_dword v109, v111, s[6:7] offset:128 nt
	global_store_dword v109, v112, s[6:7] offset:256 nt
	v_add_u32_e32 v109, 0x6000, v108
	v_add_f32_e32 v110, v105, v38
	v_add_f32_e32 v111, v106, v22
	v_add_f32_e32 v112, v107, v6
	global_store_dword v109, v110, s[6:7] nt
	global_store_dword v109, v111, s[6:7] offset:128 nt
	global_store_dword v109, v112, s[6:7] offset:256 nt
	v_add_u32_e32 v109, 0x6c00, v108
	v_add_f32_e32 v110, v105, v39
	v_add_f32_e32 v111, v106, v23
	v_add_f32_e32 v112, v107, v7
	global_store_dword v109, v110, s[6:7] nt
	global_store_dword v109, v111, s[6:7] offset:128 nt
	global_store_dword v109, v112, s[6:7] offset:256 nt
	v_add_u32_e32 v109, 0x7800, v108
	v_add_f32_e32 v110, v105, v40
	v_add_f32_e32 v111, v106, v24
	v_add_f32_e32 v112, v107, v8
	global_store_dword v109, v110, s[6:7] nt
	global_store_dword v109, v111, s[6:7] offset:128 nt
	global_store_dword v109, v112, s[6:7] offset:256 nt
	v_add_u32_e32 v109, 0x8400, v108
	v_add_f32_e32 v110, v105, v41
	v_add_f32_e32 v111, v106, v25
	v_add_f32_e32 v112, v107, v9
	global_store_dword v109, v110, s[6:7] nt
	global_store_dword v109, v111, s[6:7] offset:128 nt
	global_store_dword v109, v112, s[6:7] offset:256 nt
	v_add_u32_e32 v109, 0xc000, v108
	v_add_f32_e32 v110, v105, v42
	v_add_f32_e32 v111, v106, v26
	v_add_f32_e32 v112, v107, v10
	global_store_dword v109, v110, s[6:7] nt
	global_store_dword v109, v111, s[6:7] offset:128 nt
	global_store_dword v109, v112, s[6:7] offset:256 nt
	v_add_u32_e32 v109, 0xcc00, v108
	v_add_f32_e32 v110, v105, v43
	v_add_f32_e32 v111, v106, v27
	v_add_f32_e32 v112, v107, v11
	global_store_dword v109, v110, s[6:7] nt
	global_store_dword v109, v111, s[6:7] offset:128 nt
	global_store_dword v109, v112, s[6:7] offset:256 nt
	v_add_u32_e32 v109, 0xd800, v108
	v_add_f32_e32 v110, v105, v44
	v_add_f32_e32 v111, v106, v28
	v_add_f32_e32 v112, v107, v12
	global_store_dword v109, v110, s[6:7] nt
	global_store_dword v109, v111, s[6:7] offset:128 nt
	global_store_dword v109, v112, s[6:7] offset:256 nt
	v_add_u32_e32 v109, 0xe400, v108
	v_add_f32_e32 v110, v105, v45
	v_add_f32_e32 v111, v106, v29
	v_add_f32_e32 v112, v107, v13
	global_store_dword v109, v110, s[6:7] nt
	global_store_dword v109, v111, s[6:7] offset:128 nt
	global_store_dword v109, v112, s[6:7] offset:256 nt
	v_add_u32_e32 v109, 0x12000, v108
	v_add_f32_e32 v110, v105, v46
	v_add_f32_e32 v111, v106, v30
	v_add_f32_e32 v112, v107, v14
	global_store_dword v109, v110, s[6:7] nt
	global_store_dword v109, v111, s[6:7] offset:128 nt
	global_store_dword v109, v112, s[6:7] offset:256 nt
	v_add_u32_e32 v109, 0x12c00, v108
	v_add_f32_e32 v110, v105, v47
	v_add_f32_e32 v111, v106, v31
	v_add_f32_e32 v112, v107, v15
	global_store_dword v109, v110, s[6:7] nt
	global_store_dword v109, v111, s[6:7] offset:128 nt
	global_store_dword v109, v112, s[6:7] offset:256 nt
	v_add_u32_e32 v109, 0x13800, v108
	v_add_f32_e32 v110, v105, v48
	v_add_f32_e32 v111, v106, v32
	v_add_f32_e32 v112, v107, v16
	global_store_dword v109, v110, s[6:7] nt
	global_store_dword v109, v111, s[6:7] offset:128 nt
	global_store_dword v109, v112, s[6:7] offset:256 nt
	v_add_u32_e32 v109, 0x14400, v108
	v_add_f32_e32 v110, v105, v49
	v_add_f32_e32 v111, v106, v33
	v_add_f32_e32 v112, v107, v17
	global_store_dword v109, v110, s[6:7] nt
	global_store_dword v109, v111, s[6:7] offset:128 nt
	global_store_dword v109, v112, s[6:7] offset:256 nt
	s_endpgm
